# v30 + the last four vector-address staging loads of every K-loop also in scalar-base form (base+kstep parked in s[98:101]); padded behind the loops to v30's placement modulo 64
# speedup vs baseline: 1.0081x; 1.0015x over previous
.LBB0_119:
	ds_read_b128 v[148:151], v153
	ds_read_b128 v[156:159], v153 offset:1024
	ds_read_b128 v[160:163], v153 offset:2048
	ds_read_b128 v[164:167], v153 offset:3072
	ds_read_b128 v[168:171], v154
	ds_read_b128 v[172:175], v154 offset:1024
	ds_read_b128 v[176:179], v154 offset:2048
	ds_read_b128 v[180:183], v154 offset:3072
	s_add_u32 s24, s22, 0xfff80080
	s_addc_u32 s25, s23, -1
	s_cmp_eq_u32 s79, 28
	s_cselect_b32 s27, s15, s25
	s_cselect_b32 s26, s75, s24
	s_cselect_b32 s25, s13, s78
	s_cselect_b32 s24, s76, s77
	s_add_i32 m0, s21, 0xc000
	ds_read_b128 v[184:187], v155
	ds_read_b128 v[188:191], v155 offset:1024
	ds_read_b128 v[192:195], v155 offset:2048
	ds_read_b128 v[196:199], v155 offset:3072
	ds_read_b128 v[200:203], v155 offset:4096
	ds_read_b128 v[204:207], v155 offset:5120
	ds_read_b128 v[208:211], v155 offset:6144
	ds_read_b128 v[212:215], v155 offset:7168
	global_load_lds_dwordx4 v140, s[22:23]
	s_add_i32 m0, s21, 0xe000
	s_nop 0
	global_load_lds_dwordx4 v142, s[22:23]
	s_waitcnt vmcnt(8)
	s_waitcnt lgkmcnt(0)
	s_barrier
	s_setprio 1
	s_waitcnt lgkmcnt(0)
	v_mfma_f32_16x16x32_bf16 v[126:129], v[148:151], v[184:187], v[126:129]
	v_mfma_f32_16x16x32_bf16 v[122:125], v[160:163], v[184:187], v[122:125]
	v_mfma_f32_16x16x32_bf16 v[118:121], v[148:151], v[192:195], v[118:121]
	v_mfma_f32_16x16x32_bf16 v[110:113], v[160:163], v[192:195], v[110:113]
	v_mfma_f32_16x16x32_bf16 v[102:105], v[148:151], v[200:203], v[102:105]
	v_mfma_f32_16x16x32_bf16 v[94:97], v[160:163], v[200:203], v[94:97]
	v_mfma_f32_16x16x32_bf16 v[86:89], v[148:151], v[208:211], v[86:89]
	v_mfma_f32_16x16x32_bf16 v[78:81], v[160:163], v[208:211], v[78:81]
	v_mfma_f32_16x16x32_bf16 v[126:129], v[156:159], v[188:191], v[126:129]
	v_mfma_f32_16x16x32_bf16 v[122:125], v[164:167], v[188:191], v[122:125]
	v_mfma_f32_16x16x32_bf16 v[118:121], v[156:159], v[196:199], v[118:121]
	v_mfma_f32_16x16x32_bf16 v[110:113], v[164:167], v[196:199], v[110:113]
	v_mfma_f32_16x16x32_bf16 v[102:105], v[156:159], v[204:207], v[102:105]
	v_mfma_f32_16x16x32_bf16 v[94:97], v[164:167], v[204:207], v[94:97]
	v_mfma_f32_16x16x32_bf16 v[86:89], v[156:159], v[212:215], v[86:89]
	v_mfma_f32_16x16x32_bf16 v[78:81], v[164:167], v[212:215], v[78:81]
	s_setprio 0
	s_setprio 1
	v_mfma_f32_16x16x32_bf16 v[114:117], v[168:171], v[184:187], v[114:117]
	v_mfma_f32_16x16x32_bf16 v[106:109], v[176:179], v[184:187], v[106:109]
	v_mfma_f32_16x16x32_bf16 v[98:101], v[168:171], v[192:195], v[98:101]
	v_mfma_f32_16x16x32_bf16 v[90:93], v[176:179], v[192:195], v[90:93]
	v_mfma_f32_16x16x32_bf16 v[82:85], v[168:171], v[200:203], v[82:85]
	v_mfma_f32_16x16x32_bf16 v[74:77], v[176:179], v[200:203], v[74:77]
	v_mfma_f32_16x16x32_bf16 v[70:73], v[168:171], v[208:211], v[70:73]
	v_mfma_f32_16x16x32_bf16 v[66:69], v[176:179], v[208:211], v[66:69]
	v_mfma_f32_16x16x32_bf16 v[114:117], v[172:175], v[188:191], v[114:117]
	v_mfma_f32_16x16x32_bf16 v[106:109], v[180:183], v[188:191], v[106:109]
	v_mfma_f32_16x16x32_bf16 v[98:101], v[172:175], v[196:199], v[98:101]
	v_mfma_f32_16x16x32_bf16 v[90:93], v[180:183], v[196:199], v[90:93]
	v_mfma_f32_16x16x32_bf16 v[82:85], v[172:175], v[204:207], v[82:85]
	v_mfma_f32_16x16x32_bf16 v[74:77], v[180:183], v[204:207], v[74:77]
	v_mfma_f32_16x16x32_bf16 v[70:73], v[172:175], v[212:215], v[70:73]
	v_mfma_f32_16x16x32_bf16 v[66:69], v[180:183], v[212:215], v[66:69]
	s_setprio 0
	s_barrier
	s_add_i32 s80, s71, s33
	s_mov_b32 m0, s80
	ds_read_b128 v[184:187], v155 offset:16384
	ds_read_b128 v[188:191], v155 offset:17408
	ds_read_b128 v[192:195], v155 offset:18432
	ds_read_b128 v[196:199], v155 offset:19456
	ds_read_b128 v[200:203], v155 offset:20480
	ds_read_b128 v[204:207], v155 offset:21504
	ds_read_b128 v[208:211], v155 offset:22528
	ds_read_b128 v[212:215], v155 offset:23552
	global_load_lds_dwordx4 v136, s[24:25]
	s_add_i32 m0, s80, 0x2000
	s_add_u32 s80, s24, 0x80000
	s_addc_u32 s81, s25, 0
	s_add_i32 s82, s72, s33
	global_load_lds_dwordx4 v132, s[24:25]
	s_mov_b32 m0, s82
	s_nop 0
	global_load_lds_dwordx4 v136, s[80:81]
	s_add_i32 m0, s82, 0x2000
	s_nop 0
	global_load_lds_dwordx4 v132, s[80:81]
	s_mov_b32 m0, s21
	s_nop 0
	global_load_lds_dwordx4 v138, s[26:27]
	s_mov_b32 m0, s36
	s_nop 0
	global_load_lds_dwordx4 v134, s[26:27]
	s_add_u32 s98, s24, 0x80
	s_addc_u32 s99, s25, 0
	s_add_u32 s100, s26, 0x80
	s_addc_u32 s101, s27, 0
	s_waitcnt vmcnt(8)
	s_waitcnt lgkmcnt(0)
	s_barrier
	s_setprio 1
	s_waitcnt lgkmcnt(0)
	v_mfma_f32_16x16x32_bf16 v[62:65], v[148:151], v[184:187], v[62:65]
	v_mfma_f32_16x16x32_bf16 v[58:61], v[160:163], v[184:187], v[58:61]
	v_mfma_f32_16x16x32_bf16 v[54:57], v[148:151], v[192:195], v[54:57]
	v_mfma_f32_16x16x32_bf16 v[46:49], v[160:163], v[192:195], v[46:49]
	v_mfma_f32_16x16x32_bf16 v[38:41], v[148:151], v[200:203], v[38:41]
	v_mfma_f32_16x16x32_bf16 v[30:33], v[160:163], v[200:203], v[30:33]
	v_mfma_f32_16x16x32_bf16 v[22:25], v[148:151], v[208:211], v[22:25]
	v_mfma_f32_16x16x32_bf16 v[14:17], v[160:163], v[208:211], v[14:17]
	v_mfma_f32_16x16x32_bf16 v[62:65], v[156:159], v[188:191], v[62:65]
	v_mfma_f32_16x16x32_bf16 v[58:61], v[164:167], v[188:191], v[58:61]
	v_mfma_f32_16x16x32_bf16 v[54:57], v[156:159], v[196:199], v[54:57]
	v_mfma_f32_16x16x32_bf16 v[46:49], v[164:167], v[196:199], v[46:49]
	v_mfma_f32_16x16x32_bf16 v[38:41], v[156:159], v[204:207], v[38:41]
	v_mfma_f32_16x16x32_bf16 v[30:33], v[164:167], v[204:207], v[30:33]
	v_mfma_f32_16x16x32_bf16 v[22:25], v[156:159], v[212:215], v[22:25]
	v_mfma_f32_16x16x32_bf16 v[14:17], v[164:167], v[212:215], v[14:17]
	s_setprio 0
	s_setprio 1
	v_mfma_f32_16x16x32_bf16 v[50:53], v[168:171], v[184:187], v[50:53]
	v_mfma_f32_16x16x32_bf16 v[42:45], v[176:179], v[184:187], v[42:45]
	v_mfma_f32_16x16x32_bf16 v[34:37], v[168:171], v[192:195], v[34:37]
	v_mfma_f32_16x16x32_bf16 v[26:29], v[176:179], v[192:195], v[26:29]
	v_mfma_f32_16x16x32_bf16 v[18:21], v[168:171], v[200:203], v[18:21]
	v_mfma_f32_16x16x32_bf16 v[10:13], v[176:179], v[200:203], v[10:13]
	v_mfma_f32_16x16x32_bf16 v[6:9], v[168:171], v[208:211], v[6:9]
	v_mfma_f32_16x16x32_bf16 v[2:5], v[176:179], v[208:211], v[2:5]
	v_mfma_f32_16x16x32_bf16 v[50:53], v[172:175], v[188:191], v[50:53]
	v_mfma_f32_16x16x32_bf16 v[42:45], v[180:183], v[188:191], v[42:45]
	v_mfma_f32_16x16x32_bf16 v[34:37], v[172:175], v[196:199], v[34:37]
	v_mfma_f32_16x16x32_bf16 v[26:29], v[180:183], v[196:199], v[26:29]
	v_mfma_f32_16x16x32_bf16 v[18:21], v[172:175], v[204:207], v[18:21]
	v_mfma_f32_16x16x32_bf16 v[10:13], v[180:183], v[204:207], v[10:13]
	v_mfma_f32_16x16x32_bf16 v[6:9], v[172:175], v[212:215], v[6:9]
	v_mfma_f32_16x16x32_bf16 v[2:5], v[180:183], v[212:215], v[2:5]
	s_setprio 0
	s_barrier
	s_add_i32 s80, 0, 0x18000
	s_add_i32 s81, 0, 0x1c000
	v_add_u32_e32 v164, s80, v131
	v_add_u32_e32 v180, s81, v131
	ds_read_b128 v[148:151], v164
	ds_read_b128 v[156:159], v164 offset:1024
	ds_read_b128 v[160:163], v164 offset:2048
	ds_read_b128 v[164:167], v164 offset:3072
	ds_read_b128 v[168:171], v180
	ds_read_b128 v[172:175], v180 offset:1024
	ds_read_b128 v[176:179], v180 offset:2048
	ds_read_b128 v[180:183], v180 offset:3072
	s_add_u32 s26, s26, 0x80000
	s_addc_u32 s27, s27, 0
	s_mov_b32 m0, s37
	ds_read_b128 v[184:187], v155 offset:32768
	ds_read_b128 v[188:191], v155 offset:33792
	ds_read_b128 v[192:195], v155 offset:34816
	ds_read_b128 v[196:199], v155 offset:35840
	ds_read_b128 v[200:203], v155 offset:36864
	ds_read_b128 v[204:207], v155 offset:37888
	ds_read_b128 v[208:211], v155 offset:38912
	ds_read_b128 v[212:215], v155 offset:39936
	global_load_lds_dwordx4 v138, s[26:27]
	s_mov_b32 m0, s42
	s_nop 0
	global_load_lds_dwordx4 v134, s[26:27]
	s_waitcnt vmcnt(8)
	s_waitcnt lgkmcnt(0)
	s_barrier
	s_setprio 1
	s_waitcnt lgkmcnt(0)
	v_mfma_f32_16x16x32_bf16 v[126:129], v[148:151], v[184:187], v[126:129]
	v_mfma_f32_16x16x32_bf16 v[122:125], v[160:163], v[184:187], v[122:125]
	v_mfma_f32_16x16x32_bf16 v[118:121], v[148:151], v[192:195], v[118:121]
	v_mfma_f32_16x16x32_bf16 v[110:113], v[160:163], v[192:195], v[110:113]
	v_mfma_f32_16x16x32_bf16 v[102:105], v[148:151], v[200:203], v[102:105]
	v_mfma_f32_16x16x32_bf16 v[94:97], v[160:163], v[200:203], v[94:97]
	v_mfma_f32_16x16x32_bf16 v[86:89], v[148:151], v[208:211], v[86:89]
	v_mfma_f32_16x16x32_bf16 v[78:81], v[160:163], v[208:211], v[78:81]
	v_mfma_f32_16x16x32_bf16 v[126:129], v[156:159], v[188:191], v[126:129]
	v_mfma_f32_16x16x32_bf16 v[122:125], v[164:167], v[188:191], v[122:125]
	v_mfma_f32_16x16x32_bf16 v[118:121], v[156:159], v[196:199], v[118:121]
	v_mfma_f32_16x16x32_bf16 v[110:113], v[164:167], v[196:199], v[110:113]
	v_mfma_f32_16x16x32_bf16 v[102:105], v[156:159], v[204:207], v[102:105]
	v_mfma_f32_16x16x32_bf16 v[94:97], v[164:167], v[204:207], v[94:97]
	v_mfma_f32_16x16x32_bf16 v[86:89], v[156:159], v[212:215], v[86:89]
	v_mfma_f32_16x16x32_bf16 v[78:81], v[164:167], v[212:215], v[78:81]
	s_setprio 0
	s_setprio 1
	v_mfma_f32_16x16x32_bf16 v[114:117], v[168:171], v[184:187], v[114:117]
	v_mfma_f32_16x16x32_bf16 v[106:109], v[176:179], v[184:187], v[106:109]
	v_mfma_f32_16x16x32_bf16 v[98:101], v[168:171], v[192:195], v[98:101]
	v_mfma_f32_16x16x32_bf16 v[90:93], v[176:179], v[192:195], v[90:93]
	v_mfma_f32_16x16x32_bf16 v[82:85], v[168:171], v[200:203], v[82:85]
	v_mfma_f32_16x16x32_bf16 v[74:77], v[176:179], v[200:203], v[74:77]
	v_mfma_f32_16x16x32_bf16 v[70:73], v[168:171], v[208:211], v[70:73]
	v_mfma_f32_16x16x32_bf16 v[66:69], v[176:179], v[208:211], v[66:69]
	v_mfma_f32_16x16x32_bf16 v[114:117], v[172:175], v[188:191], v[114:117]
	v_mfma_f32_16x16x32_bf16 v[106:109], v[180:183], v[188:191], v[106:109]
	v_mfma_f32_16x16x32_bf16 v[98:101], v[172:175], v[196:199], v[98:101]
	v_mfma_f32_16x16x32_bf16 v[90:93], v[180:183], v[196:199], v[90:93]
	v_mfma_f32_16x16x32_bf16 v[82:85], v[172:175], v[204:207], v[82:85]
	v_mfma_f32_16x16x32_bf16 v[74:77], v[180:183], v[204:207], v[74:77]
	v_mfma_f32_16x16x32_bf16 v[70:73], v[172:175], v[212:215], v[70:73]
	v_mfma_f32_16x16x32_bf16 v[66:69], v[180:183], v[212:215], v[66:69]
	s_setprio 0
	s_barrier
	s_add_i32 s26, s80, s33
	s_mov_b32 m0, s26
	ds_read_b128 v[184:187], v155 offset:49152
	ds_read_b128 v[188:191], v155 offset:50176
	ds_read_b128 v[192:195], v155 offset:51200
	ds_read_b128 v[196:199], v155 offset:52224
	ds_read_b128 v[200:203], v155 offset:53248
	ds_read_b128 v[204:207], v155 offset:54272
	ds_read_b128 v[208:211], v155 offset:55296
	ds_read_b128 v[212:215], v155 offset:56320
	global_load_lds_dwordx4 v136, s[98:99]
	s_add_i32 m0, s26, 0x2000
	s_add_u32 s24, s24, 0x80080
	s_addc_u32 s25, s25, 0
	s_add_i32 s26, s81, s33
	global_load_lds_dwordx4 v132, s[98:99]
	s_mov_b32 m0, s26
	s_nop 0
	global_load_lds_dwordx4 v136, s[24:25]
	s_add_i32 m0, s26, 0x2000
	s_nop 0
	global_load_lds_dwordx4 v132, s[24:25]
	s_mov_b32 m0, s44
	s_nop 0
	global_load_lds_dwordx4 v138, s[100:101]
	s_mov_b32 m0, s45
	s_nop 0
	global_load_lds_dwordx4 v134, s[100:101]
	s_waitcnt vmcnt(8)
	s_waitcnt lgkmcnt(0)
	s_barrier
	s_setprio 1
	s_waitcnt lgkmcnt(0)
	v_mfma_f32_16x16x32_bf16 v[62:65], v[148:151], v[184:187], v[62:65]
	v_mfma_f32_16x16x32_bf16 v[58:61], v[160:163], v[184:187], v[58:61]
	v_mfma_f32_16x16x32_bf16 v[54:57], v[148:151], v[192:195], v[54:57]
	v_mfma_f32_16x16x32_bf16 v[46:49], v[160:163], v[192:195], v[46:49]
	v_mfma_f32_16x16x32_bf16 v[38:41], v[148:151], v[200:203], v[38:41]
	v_mfma_f32_16x16x32_bf16 v[30:33], v[160:163], v[200:203], v[30:33]
	v_mfma_f32_16x16x32_bf16 v[22:25], v[148:151], v[208:211], v[22:25]
	v_mfma_f32_16x16x32_bf16 v[14:17], v[160:163], v[208:211], v[14:17]
	v_mfma_f32_16x16x32_bf16 v[62:65], v[156:159], v[188:191], v[62:65]
	v_mfma_f32_16x16x32_bf16 v[58:61], v[164:167], v[188:191], v[58:61]
	v_mfma_f32_16x16x32_bf16 v[54:57], v[156:159], v[196:199], v[54:57]
	v_mfma_f32_16x16x32_bf16 v[46:49], v[164:167], v[196:199], v[46:49]
	v_mfma_f32_16x16x32_bf16 v[38:41], v[156:159], v[204:207], v[38:41]
	v_mfma_f32_16x16x32_bf16 v[30:33], v[164:167], v[204:207], v[30:33]
	v_mfma_f32_16x16x32_bf16 v[22:25], v[156:159], v[212:215], v[22:25]
	v_mfma_f32_16x16x32_bf16 v[14:17], v[164:167], v[212:215], v[14:17]
	s_setprio 0
	s_setprio 1
	v_mfma_f32_16x16x32_bf16 v[50:53], v[168:171], v[184:187], v[50:53]
	v_mfma_f32_16x16x32_bf16 v[42:45], v[176:179], v[184:187], v[42:45]
	v_mfma_f32_16x16x32_bf16 v[34:37], v[168:171], v[192:195], v[34:37]
	v_mfma_f32_16x16x32_bf16 v[26:29], v[176:179], v[192:195], v[26:29]
	v_mfma_f32_16x16x32_bf16 v[18:21], v[168:171], v[200:203], v[18:21]
	v_mfma_f32_16x16x32_bf16 v[10:13], v[176:179], v[200:203], v[10:13]
	v_mfma_f32_16x16x32_bf16 v[6:9], v[168:171], v[208:211], v[6:9]
	v_mfma_f32_16x16x32_bf16 v[2:5], v[176:179], v[208:211], v[2:5]
	v_mfma_f32_16x16x32_bf16 v[50:53], v[172:175], v[188:191], v[50:53]
	v_mfma_f32_16x16x32_bf16 v[42:45], v[180:183], v[188:191], v[42:45]
	v_mfma_f32_16x16x32_bf16 v[34:37], v[172:175], v[196:199], v[34:37]
	v_mfma_f32_16x16x32_bf16 v[26:29], v[180:183], v[196:199], v[26:29]
	v_mfma_f32_16x16x32_bf16 v[18:21], v[172:175], v[204:207], v[18:21]
	v_mfma_f32_16x16x32_bf16 v[10:13], v[180:183], v[204:207], v[10:13]
	v_mfma_f32_16x16x32_bf16 v[6:9], v[172:175], v[212:215], v[6:9]
	v_mfma_f32_16x16x32_bf16 v[2:5], v[180:183], v[212:215], v[2:5]
	s_setprio 0
	s_barrier
	s_add_i32 s79, s79, 2
	s_add_u32 s22, s22, 0x100
	s_addc_u32 s23, s23, 0
	s_add_u32 s77, s77, 0x100
	s_addc_u32 s78, s78, 0
	s_cmp_gt_u32 s79, 29
	s_cbranch_scc0 .LBB0_119
	s_nop 0
	s_nop 0
	s_nop 0
	s_nop 0
	s_nop 0
	s_nop 0
	s_nop 0
	s_nop 0
	s_nop 0
	s_and_b64 vcc, exec, s[10:11]
	s_cbranch_vccz .LBB0_122
	s_barrier

.LBB0_466:
	ds_read_b128 v[150:153], v211
	ds_read_b128 v[154:157], v211 offset:1024
	ds_read_b128 v[158:161], v211 offset:2048
	ds_read_b128 v[162:165], v211 offset:3072
	ds_read_b128 v[166:169], v212
	ds_read_b128 v[170:173], v212 offset:1024
	ds_read_b128 v[174:177], v212 offset:2048
	ds_read_b128 v[178:181], v212 offset:3072
	s_add_u32 s42, s36, 0xfff80080
	s_addc_u32 s43, s37, -1
	s_cmp_eq_u32 s83, 28
	s_cselect_b32 s45, s1, s43
	s_cselect_b32 s44, s27, s42
	s_cselect_b32 s43, s25, s63
	s_cselect_b32 s42, s35, s62
	s_add_i32 m0, s67, 0xc000
	ds_read_b128 v[182:185], v213
	ds_read_b128 v[186:189], v213 offset:1024
	ds_read_b128 v[190:193], v213 offset:2048
	ds_read_b128 v[194:197], v213 offset:3072
	ds_read_b128 v[198:201], v213 offset:4096
	ds_read_b128 v[202:205], v213 offset:5120
	ds_read_b128 v[218:221], v213 offset:6144
	ds_read_b128 v[222:225], v213 offset:7168
	global_load_lds_dwordx4 v142, s[36:37]
	s_add_i32 m0, s67, 0xe000
	s_nop 0
	global_load_lds_dwordx4 v144, s[36:37]
	s_waitcnt vmcnt(8)
	s_waitcnt lgkmcnt(0)
	s_barrier
	s_setprio 1
	s_waitcnt lgkmcnt(0)
	v_mfma_f32_16x16x32_bf16 v[126:129], v[150:153], v[182:185], v[126:129]
	v_mfma_f32_16x16x32_bf16 v[122:125], v[158:161], v[182:185], v[122:125]
	v_mfma_f32_16x16x32_bf16 v[110:113], v[150:153], v[190:193], v[110:113]
	v_mfma_f32_16x16x32_bf16 v[106:109], v[158:161], v[190:193], v[106:109]
	v_mfma_f32_16x16x32_bf16 v[94:97], v[150:153], v[198:201], v[94:97]
	v_mfma_f32_16x16x32_bf16 v[90:93], v[158:161], v[198:201], v[90:93]
	v_mfma_f32_16x16x32_bf16 v[78:81], v[150:153], v[218:221], v[78:81]
	v_mfma_f32_16x16x32_bf16 v[74:77], v[158:161], v[218:221], v[74:77]
	v_mfma_f32_16x16x32_bf16 v[126:129], v[154:157], v[186:189], v[126:129]
	v_mfma_f32_16x16x32_bf16 v[122:125], v[162:165], v[186:189], v[122:125]
	v_mfma_f32_16x16x32_bf16 v[110:113], v[154:157], v[194:197], v[110:113]
	v_mfma_f32_16x16x32_bf16 v[106:109], v[162:165], v[194:197], v[106:109]
	v_mfma_f32_16x16x32_bf16 v[94:97], v[154:157], v[202:205], v[94:97]
	v_mfma_f32_16x16x32_bf16 v[90:93], v[162:165], v[202:205], v[90:93]
	v_mfma_f32_16x16x32_bf16 v[78:81], v[154:157], v[222:225], v[78:81]
	v_mfma_f32_16x16x32_bf16 v[74:77], v[162:165], v[222:225], v[74:77]
	s_setprio 0
	s_setprio 1
	v_mfma_f32_16x16x32_bf16 v[118:121], v[166:169], v[182:185], v[118:121]
	v_mfma_f32_16x16x32_bf16 v[114:117], v[174:177], v[182:185], v[114:117]
	v_mfma_f32_16x16x32_bf16 v[102:105], v[166:169], v[190:193], v[102:105]
	v_mfma_f32_16x16x32_bf16 v[98:101], v[174:177], v[190:193], v[98:101]
	v_mfma_f32_16x16x32_bf16 v[86:89], v[166:169], v[198:201], v[86:89]
	v_mfma_f32_16x16x32_bf16 v[82:85], v[174:177], v[198:201], v[82:85]
	v_mfma_f32_16x16x32_bf16 v[70:73], v[166:169], v[218:221], v[70:73]
	v_mfma_f32_16x16x32_bf16 v[66:69], v[174:177], v[218:221], v[66:69]
	v_mfma_f32_16x16x32_bf16 v[118:121], v[170:173], v[186:189], v[118:121]
	v_mfma_f32_16x16x32_bf16 v[114:117], v[178:181], v[186:189], v[114:117]
	v_mfma_f32_16x16x32_bf16 v[102:105], v[170:173], v[194:197], v[102:105]
	v_mfma_f32_16x16x32_bf16 v[98:101], v[178:181], v[194:197], v[98:101]
	v_mfma_f32_16x16x32_bf16 v[86:89], v[170:173], v[202:205], v[86:89]
	v_mfma_f32_16x16x32_bf16 v[82:85], v[178:181], v[202:205], v[82:85]
	v_mfma_f32_16x16x32_bf16 v[70:73], v[170:173], v[222:225], v[70:73]
	v_mfma_f32_16x16x32_bf16 v[66:69], v[178:181], v[222:225], v[66:69]
	s_setprio 0
	s_barrier
	s_add_i32 s84, s79, s66
	s_mov_b32 m0, s84
	ds_read_b128 v[182:185], v213 offset:16384
	ds_read_b128 v[186:189], v213 offset:17408
	ds_read_b128 v[190:193], v213 offset:18432
	ds_read_b128 v[194:197], v213 offset:19456
	ds_read_b128 v[198:201], v213 offset:20480
	ds_read_b128 v[202:205], v213 offset:21504
	ds_read_b128 v[218:221], v213 offset:22528
	ds_read_b128 v[222:225], v213 offset:23552
	global_load_lds_dwordx4 v132, s[42:43]
	s_add_i32 m0, s84, 0x2000
	s_add_u32 s84, s42, 0x80000
	s_addc_u32 s85, s43, 0
	s_add_i32 s86, s80, s66
	global_load_lds_dwordx4 v136, s[42:43]
	s_mov_b32 m0, s86
	s_nop 0
	global_load_lds_dwordx4 v132, s[84:85]
	s_add_i32 m0, s86, 0x2000
	s_nop 0
	global_load_lds_dwordx4 v136, s[84:85]
	s_mov_b32 m0, s67
	s_nop 0
	global_load_lds_dwordx4 v130, s[44:45]
	s_mov_b32 m0, s68
	s_nop 0
	global_load_lds_dwordx4 v134, s[44:45]
	s_add_u32 s98, s42, 0x80
	s_addc_u32 s99, s43, 0
	s_add_u32 s100, s44, 0x80
	s_addc_u32 s101, s45, 0
	s_waitcnt vmcnt(8)
	s_waitcnt lgkmcnt(0)
	s_barrier
	s_setprio 1
	s_waitcnt lgkmcnt(0)
	v_mfma_f32_16x16x32_bf16 v[62:65], v[150:153], v[182:185], v[62:65]
	v_mfma_f32_16x16x32_bf16 v[58:61], v[158:161], v[182:185], v[58:61]
	v_mfma_f32_16x16x32_bf16 v[46:49], v[150:153], v[190:193], v[46:49]
	v_mfma_f32_16x16x32_bf16 v[42:45], v[158:161], v[190:193], v[42:45]
	v_mfma_f32_16x16x32_bf16 v[30:33], v[150:153], v[198:201], v[30:33]
	v_mfma_f32_16x16x32_bf16 v[26:29], v[158:161], v[198:201], v[26:29]
	v_mfma_f32_16x16x32_bf16 v[14:17], v[150:153], v[218:221], v[14:17]
	v_mfma_f32_16x16x32_bf16 v[10:13], v[158:161], v[218:221], v[10:13]
	v_mfma_f32_16x16x32_bf16 v[62:65], v[154:157], v[186:189], v[62:65]
	v_mfma_f32_16x16x32_bf16 v[58:61], v[162:165], v[186:189], v[58:61]
	v_mfma_f32_16x16x32_bf16 v[46:49], v[154:157], v[194:197], v[46:49]
	v_mfma_f32_16x16x32_bf16 v[42:45], v[162:165], v[194:197], v[42:45]
	v_mfma_f32_16x16x32_bf16 v[30:33], v[154:157], v[202:205], v[30:33]
	v_mfma_f32_16x16x32_bf16 v[26:29], v[162:165], v[202:205], v[26:29]
	v_mfma_f32_16x16x32_bf16 v[14:17], v[154:157], v[222:225], v[14:17]
	v_mfma_f32_16x16x32_bf16 v[10:13], v[162:165], v[222:225], v[10:13]
	s_setprio 0
	s_setprio 1
	v_mfma_f32_16x16x32_bf16 v[54:57], v[166:169], v[182:185], v[54:57]
	v_mfma_f32_16x16x32_bf16 v[50:53], v[174:177], v[182:185], v[50:53]
	v_mfma_f32_16x16x32_bf16 v[38:41], v[166:169], v[190:193], v[38:41]
	v_mfma_f32_16x16x32_bf16 v[34:37], v[174:177], v[190:193], v[34:37]
	v_mfma_f32_16x16x32_bf16 v[22:25], v[166:169], v[198:201], v[22:25]
	v_mfma_f32_16x16x32_bf16 v[18:21], v[174:177], v[198:201], v[18:21]
	v_mfma_f32_16x16x32_bf16 v[6:9], v[166:169], v[218:221], v[6:9]
	v_mfma_f32_16x16x32_bf16 v[2:5], v[174:177], v[218:221], v[2:5]
	v_mfma_f32_16x16x32_bf16 v[54:57], v[170:173], v[186:189], v[54:57]
	v_mfma_f32_16x16x32_bf16 v[50:53], v[178:181], v[186:189], v[50:53]
	v_mfma_f32_16x16x32_bf16 v[38:41], v[170:173], v[194:197], v[38:41]
	v_mfma_f32_16x16x32_bf16 v[34:37], v[178:181], v[194:197], v[34:37]
	v_mfma_f32_16x16x32_bf16 v[22:25], v[170:173], v[202:205], v[22:25]
	v_mfma_f32_16x16x32_bf16 v[18:21], v[178:181], v[202:205], v[18:21]
	v_mfma_f32_16x16x32_bf16 v[6:9], v[170:173], v[222:225], v[6:9]
	v_mfma_f32_16x16x32_bf16 v[2:5], v[178:181], v[222:225], v[2:5]
	s_setprio 0
	s_barrier
	s_add_i32 s84, 0, 0x18000
	v_add_u32_e32 v139, s84, v206
	s_add_i32 s85, 0, 0x1c000
	ds_read_b128 v[150:153], v139
	ds_read_b128 v[154:157], v139 offset:1024
	ds_read_b128 v[158:161], v139 offset:2048
	ds_read_b128 v[162:165], v139 offset:3072
	v_add_u32_e32 v139, s85, v206
	ds_read_b128 v[166:169], v139
	ds_read_b128 v[170:173], v139 offset:1024
	ds_read_b128 v[174:177], v139 offset:2048
	ds_read_b128 v[178:181], v139 offset:3072
	s_add_u32 s44, s44, 0x80000
	s_addc_u32 s45, s45, 0
	s_mov_b32 m0, s69
	ds_read_b128 v[182:185], v213 offset:32768
	ds_read_b128 v[186:189], v213 offset:33792
	ds_read_b128 v[190:193], v213 offset:34816
	ds_read_b128 v[194:197], v213 offset:35840
	ds_read_b128 v[198:201], v213 offset:36864
	ds_read_b128 v[202:205], v213 offset:37888
	ds_read_b128 v[218:221], v213 offset:38912
	ds_read_b128 v[222:225], v213 offset:39936
	global_load_lds_dwordx4 v130, s[44:45]
	s_mov_b32 m0, s70
	s_nop 0
	global_load_lds_dwordx4 v134, s[44:45]
	s_waitcnt vmcnt(8)
	s_waitcnt lgkmcnt(0)
	s_barrier
	s_setprio 1
	s_waitcnt lgkmcnt(0)
	v_mfma_f32_16x16x32_bf16 v[126:129], v[150:153], v[182:185], v[126:129]
	v_mfma_f32_16x16x32_bf16 v[122:125], v[158:161], v[182:185], v[122:125]
	v_mfma_f32_16x16x32_bf16 v[110:113], v[150:153], v[190:193], v[110:113]
	v_mfma_f32_16x16x32_bf16 v[106:109], v[158:161], v[190:193], v[106:109]
	v_mfma_f32_16x16x32_bf16 v[94:97], v[150:153], v[198:201], v[94:97]
	v_mfma_f32_16x16x32_bf16 v[90:93], v[158:161], v[198:201], v[90:93]
	v_mfma_f32_16x16x32_bf16 v[78:81], v[150:153], v[218:221], v[78:81]
	v_mfma_f32_16x16x32_bf16 v[74:77], v[158:161], v[218:221], v[74:77]
	v_mfma_f32_16x16x32_bf16 v[126:129], v[154:157], v[186:189], v[126:129]
	v_mfma_f32_16x16x32_bf16 v[122:125], v[162:165], v[186:189], v[122:125]
	v_mfma_f32_16x16x32_bf16 v[110:113], v[154:157], v[194:197], v[110:113]
	v_mfma_f32_16x16x32_bf16 v[106:109], v[162:165], v[194:197], v[106:109]
	v_mfma_f32_16x16x32_bf16 v[94:97], v[154:157], v[202:205], v[94:97]
	v_mfma_f32_16x16x32_bf16 v[90:93], v[162:165], v[202:205], v[90:93]
	v_mfma_f32_16x16x32_bf16 v[78:81], v[154:157], v[222:225], v[78:81]
	v_mfma_f32_16x16x32_bf16 v[74:77], v[162:165], v[222:225], v[74:77]
	s_setprio 0
	s_setprio 1
	v_mfma_f32_16x16x32_bf16 v[118:121], v[166:169], v[182:185], v[118:121]
	v_mfma_f32_16x16x32_bf16 v[114:117], v[174:177], v[182:185], v[114:117]
	v_mfma_f32_16x16x32_bf16 v[102:105], v[166:169], v[190:193], v[102:105]
	v_mfma_f32_16x16x32_bf16 v[98:101], v[174:177], v[190:193], v[98:101]
	v_mfma_f32_16x16x32_bf16 v[86:89], v[166:169], v[198:201], v[86:89]
	v_mfma_f32_16x16x32_bf16 v[82:85], v[174:177], v[198:201], v[82:85]
	v_mfma_f32_16x16x32_bf16 v[70:73], v[166:169], v[218:221], v[70:73]
	v_mfma_f32_16x16x32_bf16 v[66:69], v[174:177], v[218:221], v[66:69]
	v_mfma_f32_16x16x32_bf16 v[118:121], v[170:173], v[186:189], v[118:121]
	v_mfma_f32_16x16x32_bf16 v[114:117], v[178:181], v[186:189], v[114:117]
	v_mfma_f32_16x16x32_bf16 v[102:105], v[170:173], v[194:197], v[102:105]
	v_mfma_f32_16x16x32_bf16 v[98:101], v[178:181], v[194:197], v[98:101]
	v_mfma_f32_16x16x32_bf16 v[86:89], v[170:173], v[202:205], v[86:89]
	v_mfma_f32_16x16x32_bf16 v[82:85], v[178:181], v[202:205], v[82:85]
	v_mfma_f32_16x16x32_bf16 v[70:73], v[170:173], v[222:225], v[70:73]
	v_mfma_f32_16x16x32_bf16 v[66:69], v[178:181], v[222:225], v[66:69]
	s_setprio 0
	s_barrier
	s_add_i32 s44, s84, s66
	s_mov_b32 m0, s44
	ds_read_b128 v[182:185], v213 offset:49152
	ds_read_b128 v[186:189], v213 offset:50176
	ds_read_b128 v[190:193], v213 offset:51200
	ds_read_b128 v[194:197], v213 offset:52224
	ds_read_b128 v[198:201], v213 offset:53248
	ds_read_b128 v[202:205], v213 offset:54272
	ds_read_b128 v[218:221], v213 offset:55296
	ds_read_b128 v[222:225], v213 offset:56320
	global_load_lds_dwordx4 v132, s[98:99]
	s_add_i32 m0, s44, 0x2000
	s_add_u32 s42, s42, 0x80080
	s_addc_u32 s43, s43, 0
	s_add_i32 s44, s85, s66
	global_load_lds_dwordx4 v136, s[98:99]
	s_mov_b32 m0, s44
	s_nop 0
	global_load_lds_dwordx4 v132, s[42:43]
	s_add_i32 m0, s44, 0x2000
	s_nop 0
	global_load_lds_dwordx4 v136, s[42:43]
	s_mov_b32 m0, s74
	s_nop 0
	global_load_lds_dwordx4 v130, s[100:101]
	s_mov_b32 m0, s75
	s_nop 0
	global_load_lds_dwordx4 v134, s[100:101]
	s_waitcnt vmcnt(8)
	s_waitcnt lgkmcnt(0)
	s_barrier
	s_setprio 1
	s_waitcnt lgkmcnt(0)
	v_mfma_f32_16x16x32_bf16 v[62:65], v[150:153], v[182:185], v[62:65]
	v_mfma_f32_16x16x32_bf16 v[58:61], v[158:161], v[182:185], v[58:61]
	v_mfma_f32_16x16x32_bf16 v[46:49], v[150:153], v[190:193], v[46:49]
	v_mfma_f32_16x16x32_bf16 v[42:45], v[158:161], v[190:193], v[42:45]
	v_mfma_f32_16x16x32_bf16 v[30:33], v[150:153], v[198:201], v[30:33]
	v_mfma_f32_16x16x32_bf16 v[26:29], v[158:161], v[198:201], v[26:29]
	v_mfma_f32_16x16x32_bf16 v[14:17], v[150:153], v[218:221], v[14:17]
	v_mfma_f32_16x16x32_bf16 v[10:13], v[158:161], v[218:221], v[10:13]
	v_mfma_f32_16x16x32_bf16 v[62:65], v[154:157], v[186:189], v[62:65]
	v_mfma_f32_16x16x32_bf16 v[58:61], v[162:165], v[186:189], v[58:61]
	v_mfma_f32_16x16x32_bf16 v[46:49], v[154:157], v[194:197], v[46:49]
	v_mfma_f32_16x16x32_bf16 v[42:45], v[162:165], v[194:197], v[42:45]
	v_mfma_f32_16x16x32_bf16 v[30:33], v[154:157], v[202:205], v[30:33]
	v_mfma_f32_16x16x32_bf16 v[26:29], v[162:165], v[202:205], v[26:29]
	v_mfma_f32_16x16x32_bf16 v[14:17], v[154:157], v[222:225], v[14:17]
	v_mfma_f32_16x16x32_bf16 v[10:13], v[162:165], v[222:225], v[10:13]
	s_setprio 0
	s_setprio 1
	v_mfma_f32_16x16x32_bf16 v[54:57], v[166:169], v[182:185], v[54:57]
	v_mfma_f32_16x16x32_bf16 v[50:53], v[174:177], v[182:185], v[50:53]
	v_mfma_f32_16x16x32_bf16 v[38:41], v[166:169], v[190:193], v[38:41]
	v_mfma_f32_16x16x32_bf16 v[34:37], v[174:177], v[190:193], v[34:37]
	v_mfma_f32_16x16x32_bf16 v[22:25], v[166:169], v[198:201], v[22:25]
	v_mfma_f32_16x16x32_bf16 v[18:21], v[174:177], v[198:201], v[18:21]
	v_mfma_f32_16x16x32_bf16 v[6:9], v[166:169], v[218:221], v[6:9]
	v_mfma_f32_16x16x32_bf16 v[2:5], v[174:177], v[218:221], v[2:5]
	v_mfma_f32_16x16x32_bf16 v[54:57], v[170:173], v[186:189], v[54:57]
	v_mfma_f32_16x16x32_bf16 v[50:53], v[178:181], v[186:189], v[50:53]
	v_mfma_f32_16x16x32_bf16 v[38:41], v[170:173], v[194:197], v[38:41]
	v_mfma_f32_16x16x32_bf16 v[34:37], v[178:181], v[194:197], v[34:37]
	v_mfma_f32_16x16x32_bf16 v[22:25], v[170:173], v[202:205], v[22:25]
	v_mfma_f32_16x16x32_bf16 v[18:21], v[178:181], v[202:205], v[18:21]
	v_mfma_f32_16x16x32_bf16 v[6:9], v[170:173], v[222:225], v[6:9]
	v_mfma_f32_16x16x32_bf16 v[2:5], v[178:181], v[222:225], v[2:5]
	s_setprio 0
	s_barrier
	s_add_i32 s83, s83, 2
	s_add_u32 s36, s36, 0x100
	s_addc_u32 s37, s37, 0
	s_add_u32 s62, s62, 0x100
	s_addc_u32 s63, s63, 0
	s_cmp_gt_u32 s83, 29
	s_cbranch_scc0 .LBB0_466
	s_nop 0
	s_nop 0
	s_nop 0
	s_nop 0
	s_nop 0
	s_nop 0
	s_nop 0
	s_nop 0
	s_nop 0
	s_and_b64 vcc, exec, s[20:21]
	s_cbranch_vccz .LBB0_469
	s_barrier

.LBB0_574:
	ds_read_b128 v[146:149], v152
	ds_read_b128 v[156:159], v152 offset:1024
	ds_read_b128 v[160:163], v152 offset:2048
	ds_read_b128 v[164:167], v152 offset:3072
	ds_read_b128 v[168:171], v153
	ds_read_b128 v[172:175], v153 offset:1024
	ds_read_b128 v[176:179], v153 offset:2048
	ds_read_b128 v[180:183], v153 offset:3072
	s_add_u32 s24, s22, 0xfff80080
	s_addc_u32 s25, s23, -1
	s_cmp_eq_u32 s69, 28
	s_cselect_b32 s27, s15, s25
	s_cselect_b32 s26, s65, s24
	s_cselect_b32 s25, s13, s68
	s_cselect_b32 s24, s66, s67
	s_add_i32 m0, s21, 0xc000
	ds_read_b128 v[184:187], v154
	ds_read_b128 v[188:191], v154 offset:1024
	ds_read_b128 v[192:195], v154 offset:2048
	ds_read_b128 v[196:199], v154 offset:3072
	ds_read_b128 v[200:203], v154 offset:4096
	ds_read_b128 v[204:207], v154 offset:5120
	ds_read_b128 v[208:211], v154 offset:6144
	ds_read_b128 v[212:215], v154 offset:7168
	global_load_lds_dwordx4 v138, s[22:23]
	s_add_i32 m0, s21, 0xe000
	s_nop 0
	global_load_lds_dwordx4 v140, s[22:23]
	s_waitcnt vmcnt(8)
	s_waitcnt lgkmcnt(0)
	s_barrier
	s_setprio 1
	s_waitcnt lgkmcnt(0)
	v_mfma_f32_16x16x32_bf16 v[126:129], v[146:149], v[184:187], v[126:129]
	v_mfma_f32_16x16x32_bf16 v[122:125], v[160:163], v[184:187], v[122:125]
	v_mfma_f32_16x16x32_bf16 v[110:113], v[146:149], v[192:195], v[110:113]
	v_mfma_f32_16x16x32_bf16 v[106:109], v[160:163], v[192:195], v[106:109]
	v_mfma_f32_16x16x32_bf16 v[94:97], v[146:149], v[200:203], v[94:97]
	v_mfma_f32_16x16x32_bf16 v[90:93], v[160:163], v[200:203], v[90:93]
	v_mfma_f32_16x16x32_bf16 v[78:81], v[146:149], v[208:211], v[78:81]
	v_mfma_f32_16x16x32_bf16 v[74:77], v[160:163], v[208:211], v[74:77]
	v_mfma_f32_16x16x32_bf16 v[126:129], v[156:159], v[188:191], v[126:129]
	v_mfma_f32_16x16x32_bf16 v[122:125], v[164:167], v[188:191], v[122:125]
	v_mfma_f32_16x16x32_bf16 v[110:113], v[156:159], v[196:199], v[110:113]
	v_mfma_f32_16x16x32_bf16 v[106:109], v[164:167], v[196:199], v[106:109]
	v_mfma_f32_16x16x32_bf16 v[94:97], v[156:159], v[204:207], v[94:97]
	v_mfma_f32_16x16x32_bf16 v[90:93], v[164:167], v[204:207], v[90:93]
	v_mfma_f32_16x16x32_bf16 v[78:81], v[156:159], v[212:215], v[78:81]
	v_mfma_f32_16x16x32_bf16 v[74:77], v[164:167], v[212:215], v[74:77]
	s_setprio 0
	s_setprio 1
	v_mfma_f32_16x16x32_bf16 v[118:121], v[168:171], v[184:187], v[118:121]
	v_mfma_f32_16x16x32_bf16 v[114:117], v[176:179], v[184:187], v[114:117]
	v_mfma_f32_16x16x32_bf16 v[102:105], v[168:171], v[192:195], v[102:105]
	v_mfma_f32_16x16x32_bf16 v[98:101], v[176:179], v[192:195], v[98:101]
	v_mfma_f32_16x16x32_bf16 v[86:89], v[168:171], v[200:203], v[86:89]
	v_mfma_f32_16x16x32_bf16 v[82:85], v[176:179], v[200:203], v[82:85]
	v_mfma_f32_16x16x32_bf16 v[70:73], v[168:171], v[208:211], v[70:73]
	v_mfma_f32_16x16x32_bf16 v[66:69], v[176:179], v[208:211], v[66:69]
	v_mfma_f32_16x16x32_bf16 v[118:121], v[172:175], v[188:191], v[118:121]
	v_mfma_f32_16x16x32_bf16 v[114:117], v[180:183], v[188:191], v[114:117]
	v_mfma_f32_16x16x32_bf16 v[102:105], v[172:175], v[196:199], v[102:105]
	v_mfma_f32_16x16x32_bf16 v[98:101], v[180:183], v[196:199], v[98:101]
	v_mfma_f32_16x16x32_bf16 v[86:89], v[172:175], v[204:207], v[86:89]
	v_mfma_f32_16x16x32_bf16 v[82:85], v[180:183], v[204:207], v[82:85]
	v_mfma_f32_16x16x32_bf16 v[70:73], v[172:175], v[212:215], v[70:73]
	v_mfma_f32_16x16x32_bf16 v[66:69], v[180:183], v[212:215], v[66:69]
	s_setprio 0
	s_barrier
	s_add_i32 s70, s61, s33
	s_mov_b32 m0, s70
	ds_read_b128 v[184:187], v154 offset:16384
	ds_read_b128 v[188:191], v154 offset:17408
	ds_read_b128 v[192:195], v154 offset:18432
	ds_read_b128 v[196:199], v154 offset:19456
	ds_read_b128 v[200:203], v154 offset:20480
	ds_read_b128 v[204:207], v154 offset:21504
	ds_read_b128 v[208:211], v154 offset:22528
	ds_read_b128 v[212:215], v154 offset:23552
	global_load_lds_dwordx4 v134, s[24:25]
	s_add_i32 m0, s70, 0x2000
	s_add_u32 s70, s24, 0x80000
	s_addc_u32 s71, s25, 0
	s_add_i32 s72, s62, s33
	global_load_lds_dwordx4 v130, s[24:25]
	s_mov_b32 m0, s72
	s_nop 0
	global_load_lds_dwordx4 v134, s[70:71]
	s_add_i32 m0, s72, 0x2000
	s_nop 0
	global_load_lds_dwordx4 v130, s[70:71]
	s_mov_b32 m0, s21
	s_nop 0
	global_load_lds_dwordx4 v136, s[26:27]
	s_mov_b32 m0, s36
	s_nop 0
	global_load_lds_dwordx4 v132, s[26:27]
	s_add_u32 s98, s24, 0x80
	s_addc_u32 s99, s25, 0
	s_add_u32 s100, s26, 0x80
	s_addc_u32 s101, s27, 0
	s_waitcnt vmcnt(8)
	s_waitcnt lgkmcnt(0)
	s_barrier
	s_setprio 1
	s_waitcnt lgkmcnt(0)
	v_mfma_f32_16x16x32_bf16 v[62:65], v[146:149], v[184:187], v[62:65]
	v_mfma_f32_16x16x32_bf16 v[58:61], v[160:163], v[184:187], v[58:61]
	v_mfma_f32_16x16x32_bf16 v[46:49], v[146:149], v[192:195], v[46:49]
	v_mfma_f32_16x16x32_bf16 v[42:45], v[160:163], v[192:195], v[42:45]
	v_mfma_f32_16x16x32_bf16 v[30:33], v[146:149], v[200:203], v[30:33]
	v_mfma_f32_16x16x32_bf16 v[26:29], v[160:163], v[200:203], v[26:29]
	v_mfma_f32_16x16x32_bf16 v[14:17], v[146:149], v[208:211], v[14:17]
	v_mfma_f32_16x16x32_bf16 v[10:13], v[160:163], v[208:211], v[10:13]
	v_mfma_f32_16x16x32_bf16 v[62:65], v[156:159], v[188:191], v[62:65]
	v_mfma_f32_16x16x32_bf16 v[58:61], v[164:167], v[188:191], v[58:61]
	v_mfma_f32_16x16x32_bf16 v[46:49], v[156:159], v[196:199], v[46:49]
	v_mfma_f32_16x16x32_bf16 v[42:45], v[164:167], v[196:199], v[42:45]
	v_mfma_f32_16x16x32_bf16 v[30:33], v[156:159], v[204:207], v[30:33]
	v_mfma_f32_16x16x32_bf16 v[26:29], v[164:167], v[204:207], v[26:29]
	v_mfma_f32_16x16x32_bf16 v[14:17], v[156:159], v[212:215], v[14:17]
	v_mfma_f32_16x16x32_bf16 v[10:13], v[164:167], v[212:215], v[10:13]
	s_setprio 0
	s_setprio 1
	v_mfma_f32_16x16x32_bf16 v[54:57], v[168:171], v[184:187], v[54:57]
	v_mfma_f32_16x16x32_bf16 v[50:53], v[176:179], v[184:187], v[50:53]
	v_mfma_f32_16x16x32_bf16 v[38:41], v[168:171], v[192:195], v[38:41]
	v_mfma_f32_16x16x32_bf16 v[34:37], v[176:179], v[192:195], v[34:37]
	v_mfma_f32_16x16x32_bf16 v[22:25], v[168:171], v[200:203], v[22:25]
	v_mfma_f32_16x16x32_bf16 v[18:21], v[176:179], v[200:203], v[18:21]
	v_mfma_f32_16x16x32_bf16 v[6:9], v[168:171], v[208:211], v[6:9]
	v_mfma_f32_16x16x32_bf16 v[2:5], v[176:179], v[208:211], v[2:5]
	v_mfma_f32_16x16x32_bf16 v[54:57], v[172:175], v[188:191], v[54:57]
	v_mfma_f32_16x16x32_bf16 v[50:53], v[180:183], v[188:191], v[50:53]
	v_mfma_f32_16x16x32_bf16 v[38:41], v[172:175], v[196:199], v[38:41]
	v_mfma_f32_16x16x32_bf16 v[34:37], v[180:183], v[196:199], v[34:37]
	v_mfma_f32_16x16x32_bf16 v[22:25], v[172:175], v[204:207], v[22:25]
	v_mfma_f32_16x16x32_bf16 v[18:21], v[180:183], v[204:207], v[18:21]
	v_mfma_f32_16x16x32_bf16 v[6:9], v[172:175], v[212:215], v[6:9]
	v_mfma_f32_16x16x32_bf16 v[2:5], v[180:183], v[212:215], v[2:5]
	s_setprio 0
	s_barrier
	s_add_i32 s70, 0, 0x18000
	v_add_u32_e32 v155, s70, v150
	s_add_i32 s71, 0, 0x1c000
	ds_read_b128 v[146:149], v155
	ds_read_b128 v[156:159], v155 offset:1024
	ds_read_b128 v[160:163], v155 offset:2048
	ds_read_b128 v[164:167], v155 offset:3072
	v_add_u32_e32 v155, s71, v150
	ds_read_b128 v[168:171], v155
	ds_read_b128 v[172:175], v155 offset:1024
	ds_read_b128 v[176:179], v155 offset:2048
	ds_read_b128 v[180:183], v155 offset:3072
	s_add_u32 s26, s26, 0x80000
	s_addc_u32 s27, s27, 0
	s_mov_b32 m0, s37
	ds_read_b128 v[184:187], v154 offset:32768
	ds_read_b128 v[188:191], v154 offset:33792
	ds_read_b128 v[192:195], v154 offset:34816
	ds_read_b128 v[196:199], v154 offset:35840
	ds_read_b128 v[200:203], v154 offset:36864
	ds_read_b128 v[204:207], v154 offset:37888
	ds_read_b128 v[208:211], v154 offset:38912
	ds_read_b128 v[212:215], v154 offset:39936
	global_load_lds_dwordx4 v136, s[26:27]
	s_mov_b32 m0, s42
	s_nop 0
	global_load_lds_dwordx4 v132, s[26:27]
	s_waitcnt vmcnt(8)
	s_waitcnt lgkmcnt(0)
	s_barrier
	s_setprio 1
	s_waitcnt lgkmcnt(0)
	v_mfma_f32_16x16x32_bf16 v[126:129], v[146:149], v[184:187], v[126:129]
	v_mfma_f32_16x16x32_bf16 v[122:125], v[160:163], v[184:187], v[122:125]
	v_mfma_f32_16x16x32_bf16 v[110:113], v[146:149], v[192:195], v[110:113]
	v_mfma_f32_16x16x32_bf16 v[106:109], v[160:163], v[192:195], v[106:109]
	v_mfma_f32_16x16x32_bf16 v[94:97], v[146:149], v[200:203], v[94:97]
	v_mfma_f32_16x16x32_bf16 v[90:93], v[160:163], v[200:203], v[90:93]
	v_mfma_f32_16x16x32_bf16 v[78:81], v[146:149], v[208:211], v[78:81]
	v_mfma_f32_16x16x32_bf16 v[74:77], v[160:163], v[208:211], v[74:77]
	v_mfma_f32_16x16x32_bf16 v[126:129], v[156:159], v[188:191], v[126:129]
	v_mfma_f32_16x16x32_bf16 v[122:125], v[164:167], v[188:191], v[122:125]
	v_mfma_f32_16x16x32_bf16 v[110:113], v[156:159], v[196:199], v[110:113]
	v_mfma_f32_16x16x32_bf16 v[106:109], v[164:167], v[196:199], v[106:109]
	v_mfma_f32_16x16x32_bf16 v[94:97], v[156:159], v[204:207], v[94:97]
	v_mfma_f32_16x16x32_bf16 v[90:93], v[164:167], v[204:207], v[90:93]
	v_mfma_f32_16x16x32_bf16 v[78:81], v[156:159], v[212:215], v[78:81]
	v_mfma_f32_16x16x32_bf16 v[74:77], v[164:167], v[212:215], v[74:77]
	s_setprio 0
	s_setprio 1
	v_mfma_f32_16x16x32_bf16 v[118:121], v[168:171], v[184:187], v[118:121]
	v_mfma_f32_16x16x32_bf16 v[114:117], v[176:179], v[184:187], v[114:117]
	v_mfma_f32_16x16x32_bf16 v[102:105], v[168:171], v[192:195], v[102:105]
	v_mfma_f32_16x16x32_bf16 v[98:101], v[176:179], v[192:195], v[98:101]
	v_mfma_f32_16x16x32_bf16 v[86:89], v[168:171], v[200:203], v[86:89]
	v_mfma_f32_16x16x32_bf16 v[82:85], v[176:179], v[200:203], v[82:85]
	v_mfma_f32_16x16x32_bf16 v[70:73], v[168:171], v[208:211], v[70:73]
	v_mfma_f32_16x16x32_bf16 v[66:69], v[176:179], v[208:211], v[66:69]
	v_mfma_f32_16x16x32_bf16 v[118:121], v[172:175], v[188:191], v[118:121]
	v_mfma_f32_16x16x32_bf16 v[114:117], v[180:183], v[188:191], v[114:117]
	v_mfma_f32_16x16x32_bf16 v[102:105], v[172:175], v[196:199], v[102:105]
	v_mfma_f32_16x16x32_bf16 v[98:101], v[180:183], v[196:199], v[98:101]
	v_mfma_f32_16x16x32_bf16 v[86:89], v[172:175], v[204:207], v[86:89]
	v_mfma_f32_16x16x32_bf16 v[82:85], v[180:183], v[204:207], v[82:85]
	v_mfma_f32_16x16x32_bf16 v[70:73], v[172:175], v[212:215], v[70:73]
	v_mfma_f32_16x16x32_bf16 v[66:69], v[180:183], v[212:215], v[66:69]
	s_setprio 0
	s_barrier
	s_add_i32 s26, s70, s33
	s_mov_b32 m0, s26
	ds_read_b128 v[184:187], v154 offset:49152
	ds_read_b128 v[188:191], v154 offset:50176
	ds_read_b128 v[192:195], v154 offset:51200
	ds_read_b128 v[196:199], v154 offset:52224
	ds_read_b128 v[200:203], v154 offset:53248
	ds_read_b128 v[204:207], v154 offset:54272
	ds_read_b128 v[208:211], v154 offset:55296
	ds_read_b128 v[212:215], v154 offset:56320
	global_load_lds_dwordx4 v134, s[98:99]
	s_add_i32 m0, s26, 0x2000
	s_add_u32 s24, s24, 0x80080
	s_addc_u32 s25, s25, 0
	s_add_i32 s26, s71, s33
	global_load_lds_dwordx4 v130, s[98:99]
	s_mov_b32 m0, s26
	s_nop 0
	global_load_lds_dwordx4 v134, s[24:25]
	s_add_i32 m0, s26, 0x2000
	s_nop 0
	global_load_lds_dwordx4 v130, s[24:25]
	s_mov_b32 m0, s44
	s_nop 0
	global_load_lds_dwordx4 v136, s[100:101]
	s_mov_b32 m0, s45
	s_nop 0
	global_load_lds_dwordx4 v132, s[100:101]
	s_waitcnt vmcnt(8)
	s_waitcnt lgkmcnt(0)
	s_barrier
	s_setprio 1
	s_waitcnt lgkmcnt(0)
	v_mfma_f32_16x16x32_bf16 v[62:65], v[146:149], v[184:187], v[62:65]
	v_mfma_f32_16x16x32_bf16 v[58:61], v[160:163], v[184:187], v[58:61]
	v_mfma_f32_16x16x32_bf16 v[46:49], v[146:149], v[192:195], v[46:49]
	v_mfma_f32_16x16x32_bf16 v[42:45], v[160:163], v[192:195], v[42:45]
	v_mfma_f32_16x16x32_bf16 v[30:33], v[146:149], v[200:203], v[30:33]
	v_mfma_f32_16x16x32_bf16 v[26:29], v[160:163], v[200:203], v[26:29]
	v_mfma_f32_16x16x32_bf16 v[14:17], v[146:149], v[208:211], v[14:17]
	v_mfma_f32_16x16x32_bf16 v[10:13], v[160:163], v[208:211], v[10:13]
	v_mfma_f32_16x16x32_bf16 v[62:65], v[156:159], v[188:191], v[62:65]
	v_mfma_f32_16x16x32_bf16 v[58:61], v[164:167], v[188:191], v[58:61]
	v_mfma_f32_16x16x32_bf16 v[46:49], v[156:159], v[196:199], v[46:49]
	v_mfma_f32_16x16x32_bf16 v[42:45], v[164:167], v[196:199], v[42:45]
	v_mfma_f32_16x16x32_bf16 v[30:33], v[156:159], v[204:207], v[30:33]
	v_mfma_f32_16x16x32_bf16 v[26:29], v[164:167], v[204:207], v[26:29]
	v_mfma_f32_16x16x32_bf16 v[14:17], v[156:159], v[212:215], v[14:17]
	v_mfma_f32_16x16x32_bf16 v[10:13], v[164:167], v[212:215], v[10:13]
	s_setprio 0
	s_setprio 1
	v_mfma_f32_16x16x32_bf16 v[54:57], v[168:171], v[184:187], v[54:57]
	v_mfma_f32_16x16x32_bf16 v[50:53], v[176:179], v[184:187], v[50:53]
	v_mfma_f32_16x16x32_bf16 v[38:41], v[168:171], v[192:195], v[38:41]
	v_mfma_f32_16x16x32_bf16 v[34:37], v[176:179], v[192:195], v[34:37]
	v_mfma_f32_16x16x32_bf16 v[22:25], v[168:171], v[200:203], v[22:25]
	v_mfma_f32_16x16x32_bf16 v[18:21], v[176:179], v[200:203], v[18:21]
	v_mfma_f32_16x16x32_bf16 v[6:9], v[168:171], v[208:211], v[6:9]
	v_mfma_f32_16x16x32_bf16 v[2:5], v[176:179], v[208:211], v[2:5]
	v_mfma_f32_16x16x32_bf16 v[54:57], v[172:175], v[188:191], v[54:57]
	v_mfma_f32_16x16x32_bf16 v[50:53], v[180:183], v[188:191], v[50:53]
	v_mfma_f32_16x16x32_bf16 v[38:41], v[172:175], v[196:199], v[38:41]
	v_mfma_f32_16x16x32_bf16 v[34:37], v[180:183], v[196:199], v[34:37]
	v_mfma_f32_16x16x32_bf16 v[22:25], v[172:175], v[204:207], v[22:25]
	v_mfma_f32_16x16x32_bf16 v[18:21], v[180:183], v[204:207], v[18:21]
	v_mfma_f32_16x16x32_bf16 v[6:9], v[172:175], v[212:215], v[6:9]
	v_mfma_f32_16x16x32_bf16 v[2:5], v[180:183], v[212:215], v[2:5]
	s_setprio 0
	s_barrier
	s_add_i32 s69, s69, 2
	s_add_u32 s22, s22, 0x100
	s_addc_u32 s23, s23, 0
	s_add_u32 s67, s67, 0x100
	s_addc_u32 s68, s68, 0
	s_cmp_gt_u32 s69, 29
	s_cbranch_scc0 .LBB0_574
	s_nop 0
	s_nop 0
	s_nop 0
	s_nop 0
	s_nop 0
	s_nop 0
	s_nop 0
	s_nop 0
	s_nop 0
	s_and_b64 vcc, exec, s[10:11]
	s_cbranch_vccz .LBB0_577
	s_barrier

.LBB0_659:
	ds_read_b128 v[150:153], v211
	ds_read_b128 v[154:157], v211 offset:1024
	ds_read_b128 v[158:161], v211 offset:2048
	ds_read_b128 v[162:165], v211 offset:3072
	ds_read_b128 v[166:169], v212
	ds_read_b128 v[170:173], v212 offset:1024
	ds_read_b128 v[174:177], v212 offset:2048
	ds_read_b128 v[178:181], v212 offset:3072
	s_add_u32 s36, s0, 0xffea8080
	s_addc_u32 s37, s1, -1
	s_cmpk_eq_i32 s44, 0x52
	s_cselect_b32 s43, s27, s37
	s_cselect_b32 s42, s26, s36
	s_cselect_b32 s37, s29, s35
	s_cselect_b32 s36, s28, s31
	s_add_i32 m0, s63, 0xc000
	ds_read_b128 v[182:185], v213
	ds_read_b128 v[186:189], v213 offset:1024
	ds_read_b128 v[190:193], v213 offset:2048
	ds_read_b128 v[194:197], v213 offset:3072
	ds_read_b128 v[198:201], v213 offset:4096
	ds_read_b128 v[202:205], v213 offset:5120
	ds_read_b128 v[218:221], v213 offset:6144
	ds_read_b128 v[222:225], v213 offset:7168
	global_load_lds_dwordx4 v142, s[0:1]
	s_add_i32 m0, s63, 0xe000
	s_nop 0
	global_load_lds_dwordx4 v144, s[0:1]
	s_waitcnt vmcnt(8)
	s_waitcnt lgkmcnt(0)
	s_barrier
	s_setprio 1
	s_waitcnt lgkmcnt(0)
	v_mfma_f32_16x16x32_bf16 v[126:129], v[150:153], v[182:185], v[126:129]
	v_mfma_f32_16x16x32_bf16 v[122:125], v[158:161], v[182:185], v[122:125]
	v_mfma_f32_16x16x32_bf16 v[110:113], v[150:153], v[190:193], v[110:113]
	v_mfma_f32_16x16x32_bf16 v[106:109], v[158:161], v[190:193], v[106:109]
	v_mfma_f32_16x16x32_bf16 v[94:97], v[150:153], v[198:201], v[94:97]
	v_mfma_f32_16x16x32_bf16 v[90:93], v[158:161], v[198:201], v[90:93]
	v_mfma_f32_16x16x32_bf16 v[78:81], v[150:153], v[218:221], v[78:81]
	v_mfma_f32_16x16x32_bf16 v[74:77], v[158:161], v[218:221], v[74:77]
	v_mfma_f32_16x16x32_bf16 v[126:129], v[154:157], v[186:189], v[126:129]
	v_mfma_f32_16x16x32_bf16 v[122:125], v[162:165], v[186:189], v[122:125]
	v_mfma_f32_16x16x32_bf16 v[110:113], v[154:157], v[194:197], v[110:113]
	v_mfma_f32_16x16x32_bf16 v[106:109], v[162:165], v[194:197], v[106:109]
	v_mfma_f32_16x16x32_bf16 v[94:97], v[154:157], v[202:205], v[94:97]
	v_mfma_f32_16x16x32_bf16 v[90:93], v[162:165], v[202:205], v[90:93]
	v_mfma_f32_16x16x32_bf16 v[78:81], v[154:157], v[222:225], v[78:81]
	v_mfma_f32_16x16x32_bf16 v[74:77], v[162:165], v[222:225], v[74:77]
	s_setprio 0
	s_setprio 1
	v_mfma_f32_16x16x32_bf16 v[118:121], v[166:169], v[182:185], v[118:121]
	v_mfma_f32_16x16x32_bf16 v[114:117], v[174:177], v[182:185], v[114:117]
	v_mfma_f32_16x16x32_bf16 v[102:105], v[166:169], v[190:193], v[102:105]
	v_mfma_f32_16x16x32_bf16 v[98:101], v[174:177], v[190:193], v[98:101]
	v_mfma_f32_16x16x32_bf16 v[86:89], v[166:169], v[198:201], v[86:89]
	v_mfma_f32_16x16x32_bf16 v[82:85], v[174:177], v[198:201], v[82:85]
	v_mfma_f32_16x16x32_bf16 v[70:73], v[166:169], v[218:221], v[70:73]
	v_mfma_f32_16x16x32_bf16 v[66:69], v[174:177], v[218:221], v[66:69]
	v_mfma_f32_16x16x32_bf16 v[118:121], v[170:173], v[186:189], v[118:121]
	v_mfma_f32_16x16x32_bf16 v[114:117], v[178:181], v[186:189], v[114:117]
	v_mfma_f32_16x16x32_bf16 v[102:105], v[170:173], v[194:197], v[102:105]
	v_mfma_f32_16x16x32_bf16 v[98:101], v[178:181], v[194:197], v[98:101]
	v_mfma_f32_16x16x32_bf16 v[86:89], v[170:173], v[202:205], v[86:89]
	v_mfma_f32_16x16x32_bf16 v[82:85], v[178:181], v[202:205], v[82:85]
	v_mfma_f32_16x16x32_bf16 v[70:73], v[170:173], v[222:225], v[70:73]
	v_mfma_f32_16x16x32_bf16 v[66:69], v[178:181], v[222:225], v[66:69]
	s_setprio 0
	s_barrier
	s_add_i32 s45, s75, s62
	s_mov_b32 m0, s45
	ds_read_b128 v[182:185], v213 offset:16384
	ds_read_b128 v[186:189], v213 offset:17408
	ds_read_b128 v[190:193], v213 offset:18432
	ds_read_b128 v[194:197], v213 offset:19456
	ds_read_b128 v[198:201], v213 offset:20480
	ds_read_b128 v[202:205], v213 offset:21504
	ds_read_b128 v[218:221], v213 offset:22528
	ds_read_b128 v[222:225], v213 offset:23552
	global_load_lds_dwordx4 v132, s[36:37]
	s_add_i32 m0, s45, 0x2000
	s_add_u32 s82, s36, 0x158000
	s_addc_u32 s83, s37, 0
	s_add_i32 s45, s76, s62
	global_load_lds_dwordx4 v136, s[36:37]
	s_mov_b32 m0, s45
	s_nop 0
	global_load_lds_dwordx4 v132, s[82:83]
	s_add_i32 m0, s45, 0x2000
	s_nop 0
	global_load_lds_dwordx4 v136, s[82:83]
	s_mov_b32 m0, s63
	s_nop 0
	global_load_lds_dwordx4 v130, s[42:43]
	s_mov_b32 m0, s64
	s_nop 0
	global_load_lds_dwordx4 v134, s[42:43]
	s_add_u32 s98, s36, 0x80
	s_addc_u32 s99, s37, 0
	s_add_u32 s100, s42, 0x80
	s_addc_u32 s101, s43, 0
	s_waitcnt vmcnt(8)
	s_waitcnt lgkmcnt(0)
	s_barrier
	s_setprio 1
	s_waitcnt lgkmcnt(0)
	v_mfma_f32_16x16x32_bf16 v[62:65], v[150:153], v[182:185], v[62:65]
	v_mfma_f32_16x16x32_bf16 v[58:61], v[158:161], v[182:185], v[58:61]
	v_mfma_f32_16x16x32_bf16 v[46:49], v[150:153], v[190:193], v[46:49]
	v_mfma_f32_16x16x32_bf16 v[42:45], v[158:161], v[190:193], v[42:45]
	v_mfma_f32_16x16x32_bf16 v[30:33], v[150:153], v[198:201], v[30:33]
	v_mfma_f32_16x16x32_bf16 v[26:29], v[158:161], v[198:201], v[26:29]
	v_mfma_f32_16x16x32_bf16 v[14:17], v[150:153], v[218:221], v[14:17]
	v_mfma_f32_16x16x32_bf16 v[10:13], v[158:161], v[218:221], v[10:13]
	v_mfma_f32_16x16x32_bf16 v[62:65], v[154:157], v[186:189], v[62:65]
	v_mfma_f32_16x16x32_bf16 v[58:61], v[162:165], v[186:189], v[58:61]
	v_mfma_f32_16x16x32_bf16 v[46:49], v[154:157], v[194:197], v[46:49]
	v_mfma_f32_16x16x32_bf16 v[42:45], v[162:165], v[194:197], v[42:45]
	v_mfma_f32_16x16x32_bf16 v[30:33], v[154:157], v[202:205], v[30:33]
	v_mfma_f32_16x16x32_bf16 v[26:29], v[162:165], v[202:205], v[26:29]
	v_mfma_f32_16x16x32_bf16 v[14:17], v[154:157], v[222:225], v[14:17]
	v_mfma_f32_16x16x32_bf16 v[10:13], v[162:165], v[222:225], v[10:13]
	s_setprio 0
	s_setprio 1
	v_mfma_f32_16x16x32_bf16 v[54:57], v[166:169], v[182:185], v[54:57]
	v_mfma_f32_16x16x32_bf16 v[50:53], v[174:177], v[182:185], v[50:53]
	v_mfma_f32_16x16x32_bf16 v[38:41], v[166:169], v[190:193], v[38:41]
	v_mfma_f32_16x16x32_bf16 v[34:37], v[174:177], v[190:193], v[34:37]
	v_mfma_f32_16x16x32_bf16 v[22:25], v[166:169], v[198:201], v[22:25]
	v_mfma_f32_16x16x32_bf16 v[18:21], v[174:177], v[198:201], v[18:21]
	v_mfma_f32_16x16x32_bf16 v[6:9], v[166:169], v[218:221], v[6:9]
	v_mfma_f32_16x16x32_bf16 v[2:5], v[174:177], v[218:221], v[2:5]
	v_mfma_f32_16x16x32_bf16 v[54:57], v[170:173], v[186:189], v[54:57]
	v_mfma_f32_16x16x32_bf16 v[50:53], v[178:181], v[186:189], v[50:53]
	v_mfma_f32_16x16x32_bf16 v[38:41], v[170:173], v[194:197], v[38:41]
	v_mfma_f32_16x16x32_bf16 v[34:37], v[178:181], v[194:197], v[34:37]
	v_mfma_f32_16x16x32_bf16 v[22:25], v[170:173], v[202:205], v[22:25]
	v_mfma_f32_16x16x32_bf16 v[18:21], v[178:181], v[202:205], v[18:21]
	v_mfma_f32_16x16x32_bf16 v[6:9], v[170:173], v[222:225], v[6:9]
	v_mfma_f32_16x16x32_bf16 v[2:5], v[178:181], v[222:225], v[2:5]
	s_setprio 0
	s_barrier
	s_add_i32 s45, 0, 0x18000
	v_add_u32_e32 v139, s45, v206
	s_add_i32 s81, 0, 0x1c000
	ds_read_b128 v[150:153], v139
	ds_read_b128 v[154:157], v139 offset:1024
	ds_read_b128 v[158:161], v139 offset:2048
	ds_read_b128 v[162:165], v139 offset:3072
	v_add_u32_e32 v139, s81, v206
	ds_read_b128 v[166:169], v139
	ds_read_b128 v[170:173], v139 offset:1024
	ds_read_b128 v[174:177], v139 offset:2048
	ds_read_b128 v[178:181], v139 offset:3072
	s_add_u32 s42, s42, 0x158000
	s_addc_u32 s43, s43, 0
	s_mov_b32 m0, s65
	ds_read_b128 v[182:185], v213 offset:32768
	ds_read_b128 v[186:189], v213 offset:33792
	ds_read_b128 v[190:193], v213 offset:34816
	ds_read_b128 v[194:197], v213 offset:35840
	ds_read_b128 v[198:201], v213 offset:36864
	ds_read_b128 v[202:205], v213 offset:37888
	ds_read_b128 v[218:221], v213 offset:38912
	ds_read_b128 v[222:225], v213 offset:39936
	global_load_lds_dwordx4 v130, s[42:43]
	s_mov_b32 m0, s66
	s_nop 0
	global_load_lds_dwordx4 v134, s[42:43]
	s_waitcnt vmcnt(8)
	s_waitcnt lgkmcnt(0)
	s_barrier
	s_setprio 1
	s_waitcnt lgkmcnt(0)
	v_mfma_f32_16x16x32_bf16 v[126:129], v[150:153], v[182:185], v[126:129]
	v_mfma_f32_16x16x32_bf16 v[122:125], v[158:161], v[182:185], v[122:125]
	v_mfma_f32_16x16x32_bf16 v[110:113], v[150:153], v[190:193], v[110:113]
	v_mfma_f32_16x16x32_bf16 v[106:109], v[158:161], v[190:193], v[106:109]
	v_mfma_f32_16x16x32_bf16 v[94:97], v[150:153], v[198:201], v[94:97]
	v_mfma_f32_16x16x32_bf16 v[90:93], v[158:161], v[198:201], v[90:93]
	v_mfma_f32_16x16x32_bf16 v[78:81], v[150:153], v[218:221], v[78:81]
	v_mfma_f32_16x16x32_bf16 v[74:77], v[158:161], v[218:221], v[74:77]
	v_mfma_f32_16x16x32_bf16 v[126:129], v[154:157], v[186:189], v[126:129]
	v_mfma_f32_16x16x32_bf16 v[122:125], v[162:165], v[186:189], v[122:125]
	v_mfma_f32_16x16x32_bf16 v[110:113], v[154:157], v[194:197], v[110:113]
	v_mfma_f32_16x16x32_bf16 v[106:109], v[162:165], v[194:197], v[106:109]
	v_mfma_f32_16x16x32_bf16 v[94:97], v[154:157], v[202:205], v[94:97]
	v_mfma_f32_16x16x32_bf16 v[90:93], v[162:165], v[202:205], v[90:93]
	v_mfma_f32_16x16x32_bf16 v[78:81], v[154:157], v[222:225], v[78:81]
	v_mfma_f32_16x16x32_bf16 v[74:77], v[162:165], v[222:225], v[74:77]
	s_setprio 0
	s_setprio 1
	v_mfma_f32_16x16x32_bf16 v[118:121], v[166:169], v[182:185], v[118:121]
	v_mfma_f32_16x16x32_bf16 v[114:117], v[174:177], v[182:185], v[114:117]
	v_mfma_f32_16x16x32_bf16 v[102:105], v[166:169], v[190:193], v[102:105]
	v_mfma_f32_16x16x32_bf16 v[98:101], v[174:177], v[190:193], v[98:101]
	v_mfma_f32_16x16x32_bf16 v[86:89], v[166:169], v[198:201], v[86:89]
	v_mfma_f32_16x16x32_bf16 v[82:85], v[174:177], v[198:201], v[82:85]
	v_mfma_f32_16x16x32_bf16 v[70:73], v[166:169], v[218:221], v[70:73]
	v_mfma_f32_16x16x32_bf16 v[66:69], v[174:177], v[218:221], v[66:69]
	v_mfma_f32_16x16x32_bf16 v[118:121], v[170:173], v[186:189], v[118:121]
	v_mfma_f32_16x16x32_bf16 v[114:117], v[178:181], v[186:189], v[114:117]
	v_mfma_f32_16x16x32_bf16 v[102:105], v[170:173], v[194:197], v[102:105]
	v_mfma_f32_16x16x32_bf16 v[98:101], v[178:181], v[194:197], v[98:101]
	v_mfma_f32_16x16x32_bf16 v[86:89], v[170:173], v[202:205], v[86:89]
	v_mfma_f32_16x16x32_bf16 v[82:85], v[178:181], v[202:205], v[82:85]
	v_mfma_f32_16x16x32_bf16 v[70:73], v[170:173], v[222:225], v[70:73]
	v_mfma_f32_16x16x32_bf16 v[66:69], v[178:181], v[222:225], v[66:69]
	s_setprio 0
	s_barrier
	s_add_i32 s42, s45, s62
	s_mov_b32 m0, s42
	ds_read_b128 v[182:185], v213 offset:49152
	ds_read_b128 v[186:189], v213 offset:50176
	ds_read_b128 v[190:193], v213 offset:51200
	ds_read_b128 v[194:197], v213 offset:52224
	ds_read_b128 v[198:201], v213 offset:53248
	ds_read_b128 v[202:205], v213 offset:54272
	ds_read_b128 v[218:221], v213 offset:55296
	ds_read_b128 v[222:225], v213 offset:56320
	global_load_lds_dwordx4 v132, s[98:99]
	s_add_i32 m0, s42, 0x2000
	s_add_u32 s36, s36, 0x158080
	s_addc_u32 s37, s37, 0
	s_add_i32 s42, s81, s62
	global_load_lds_dwordx4 v136, s[98:99]
	s_mov_b32 m0, s42
	s_nop 0
	global_load_lds_dwordx4 v132, s[36:37]
	s_add_i32 m0, s42, 0x2000
	s_nop 0
	global_load_lds_dwordx4 v136, s[36:37]
	s_mov_b32 m0, s70
	s_nop 0
	global_load_lds_dwordx4 v130, s[100:101]
	s_mov_b32 m0, s71
	s_nop 0
	global_load_lds_dwordx4 v134, s[100:101]
	s_waitcnt vmcnt(8)
	s_waitcnt lgkmcnt(0)
	s_barrier
	s_setprio 1
	s_waitcnt lgkmcnt(0)
	v_mfma_f32_16x16x32_bf16 v[62:65], v[150:153], v[182:185], v[62:65]
	v_mfma_f32_16x16x32_bf16 v[58:61], v[158:161], v[182:185], v[58:61]
	v_mfma_f32_16x16x32_bf16 v[46:49], v[150:153], v[190:193], v[46:49]
	v_mfma_f32_16x16x32_bf16 v[42:45], v[158:161], v[190:193], v[42:45]
	v_mfma_f32_16x16x32_bf16 v[30:33], v[150:153], v[198:201], v[30:33]
	v_mfma_f32_16x16x32_bf16 v[26:29], v[158:161], v[198:201], v[26:29]
	v_mfma_f32_16x16x32_bf16 v[14:17], v[150:153], v[218:221], v[14:17]
	v_mfma_f32_16x16x32_bf16 v[10:13], v[158:161], v[218:221], v[10:13]
	v_mfma_f32_16x16x32_bf16 v[62:65], v[154:157], v[186:189], v[62:65]
	v_mfma_f32_16x16x32_bf16 v[58:61], v[162:165], v[186:189], v[58:61]
	v_mfma_f32_16x16x32_bf16 v[46:49], v[154:157], v[194:197], v[46:49]
	v_mfma_f32_16x16x32_bf16 v[42:45], v[162:165], v[194:197], v[42:45]
	v_mfma_f32_16x16x32_bf16 v[30:33], v[154:157], v[202:205], v[30:33]
	v_mfma_f32_16x16x32_bf16 v[26:29], v[162:165], v[202:205], v[26:29]
	v_mfma_f32_16x16x32_bf16 v[14:17], v[154:157], v[222:225], v[14:17]
	v_mfma_f32_16x16x32_bf16 v[10:13], v[162:165], v[222:225], v[10:13]
	s_setprio 0
	s_setprio 1
	v_mfma_f32_16x16x32_bf16 v[54:57], v[166:169], v[182:185], v[54:57]
	v_mfma_f32_16x16x32_bf16 v[50:53], v[174:177], v[182:185], v[50:53]
	v_mfma_f32_16x16x32_bf16 v[38:41], v[166:169], v[190:193], v[38:41]
	v_mfma_f32_16x16x32_bf16 v[34:37], v[174:177], v[190:193], v[34:37]
	v_mfma_f32_16x16x32_bf16 v[22:25], v[166:169], v[198:201], v[22:25]
	v_mfma_f32_16x16x32_bf16 v[18:21], v[174:177], v[198:201], v[18:21]
	v_mfma_f32_16x16x32_bf16 v[6:9], v[166:169], v[218:221], v[6:9]
	v_mfma_f32_16x16x32_bf16 v[2:5], v[174:177], v[218:221], v[2:5]
	v_mfma_f32_16x16x32_bf16 v[54:57], v[170:173], v[186:189], v[54:57]
	v_mfma_f32_16x16x32_bf16 v[50:53], v[178:181], v[186:189], v[50:53]
	v_mfma_f32_16x16x32_bf16 v[38:41], v[170:173], v[194:197], v[38:41]
	v_mfma_f32_16x16x32_bf16 v[34:37], v[178:181], v[194:197], v[34:37]
	v_mfma_f32_16x16x32_bf16 v[22:25], v[170:173], v[202:205], v[22:25]
	v_mfma_f32_16x16x32_bf16 v[18:21], v[178:181], v[202:205], v[18:21]
	v_mfma_f32_16x16x32_bf16 v[6:9], v[170:173], v[222:225], v[6:9]
	v_mfma_f32_16x16x32_bf16 v[2:5], v[178:181], v[222:225], v[2:5]
	s_setprio 0
	s_barrier
	s_add_i32 s44, s44, 2
	s_add_u32 s0, s0, 0x100
	s_addc_u32 s1, s1, 0
	s_add_u32 s31, s31, 0x100
	s_addc_u32 s35, s35, 0
	s_cmpk_gt_u32 s44, 0x53
	s_cbranch_scc0 .LBB0_659
	s_nop 0
	s_nop 0
	s_nop 0
	s_nop 0
	s_nop 0
	s_nop 0
	s_nop 0
	s_nop 0
	s_nop 0
	s_and_b64 vcc, exec, s[22:23]
	s_cbranch_vccz .LBB0_662
	s_barrier

.LBB0_767:
	ds_read_b128 v[146:149], v152
	ds_read_b128 v[156:159], v152 offset:1024
	ds_read_b128 v[160:163], v152 offset:2048
	ds_read_b128 v[164:167], v152 offset:3072
	ds_read_b128 v[168:171], v153
	ds_read_b128 v[172:175], v153 offset:1024
	ds_read_b128 v[176:179], v153 offset:2048
	ds_read_b128 v[180:183], v153 offset:3072
	s_add_u32 s24, s22, 0xfff80080
	s_addc_u32 s25, s23, -1
	s_cmp_eq_u32 s69, 28
	s_cselect_b32 s27, s15, s25
	s_cselect_b32 s26, s65, s24
	s_cselect_b32 s25, s13, s68
	s_cselect_b32 s24, s66, s67
	s_add_i32 m0, s21, 0xc000
	ds_read_b128 v[184:187], v154
	ds_read_b128 v[188:191], v154 offset:1024
	ds_read_b128 v[192:195], v154 offset:2048
	ds_read_b128 v[196:199], v154 offset:3072
	ds_read_b128 v[200:203], v154 offset:4096
	ds_read_b128 v[204:207], v154 offset:5120
	ds_read_b128 v[208:211], v154 offset:6144
	ds_read_b128 v[212:215], v154 offset:7168
	global_load_lds_dwordx4 v138, s[22:23]
	s_add_i32 m0, s21, 0xe000
	s_nop 0
	global_load_lds_dwordx4 v140, s[22:23]
	s_waitcnt vmcnt(8)
	s_waitcnt lgkmcnt(0)
	s_barrier
	s_setprio 1
	s_waitcnt lgkmcnt(0)
	v_mfma_f32_16x16x32_bf16 v[126:129], v[146:149], v[184:187], v[126:129]
	v_mfma_f32_16x16x32_bf16 v[122:125], v[160:163], v[184:187], v[122:125]
	v_mfma_f32_16x16x32_bf16 v[118:121], v[146:149], v[192:195], v[118:121]
	v_mfma_f32_16x16x32_bf16 v[110:113], v[160:163], v[192:195], v[110:113]
	v_mfma_f32_16x16x32_bf16 v[102:105], v[146:149], v[200:203], v[102:105]
	v_mfma_f32_16x16x32_bf16 v[94:97], v[160:163], v[200:203], v[94:97]
	v_mfma_f32_16x16x32_bf16 v[86:89], v[146:149], v[208:211], v[86:89]
	v_mfma_f32_16x16x32_bf16 v[78:81], v[160:163], v[208:211], v[78:81]
	v_mfma_f32_16x16x32_bf16 v[126:129], v[156:159], v[188:191], v[126:129]
	v_mfma_f32_16x16x32_bf16 v[122:125], v[164:167], v[188:191], v[122:125]
	v_mfma_f32_16x16x32_bf16 v[118:121], v[156:159], v[196:199], v[118:121]
	v_mfma_f32_16x16x32_bf16 v[110:113], v[164:167], v[196:199], v[110:113]
	v_mfma_f32_16x16x32_bf16 v[102:105], v[156:159], v[204:207], v[102:105]
	v_mfma_f32_16x16x32_bf16 v[94:97], v[164:167], v[204:207], v[94:97]
	v_mfma_f32_16x16x32_bf16 v[86:89], v[156:159], v[212:215], v[86:89]
	v_mfma_f32_16x16x32_bf16 v[78:81], v[164:167], v[212:215], v[78:81]
	s_setprio 0
	s_setprio 1
	v_mfma_f32_16x16x32_bf16 v[114:117], v[168:171], v[184:187], v[114:117]
	v_mfma_f32_16x16x32_bf16 v[106:109], v[176:179], v[184:187], v[106:109]
	v_mfma_f32_16x16x32_bf16 v[98:101], v[168:171], v[192:195], v[98:101]
	v_mfma_f32_16x16x32_bf16 v[90:93], v[176:179], v[192:195], v[90:93]
	v_mfma_f32_16x16x32_bf16 v[82:85], v[168:171], v[200:203], v[82:85]
	v_mfma_f32_16x16x32_bf16 v[74:77], v[176:179], v[200:203], v[74:77]
	v_mfma_f32_16x16x32_bf16 v[70:73], v[168:171], v[208:211], v[70:73]
	v_mfma_f32_16x16x32_bf16 v[66:69], v[176:179], v[208:211], v[66:69]
	v_mfma_f32_16x16x32_bf16 v[114:117], v[172:175], v[188:191], v[114:117]
	v_mfma_f32_16x16x32_bf16 v[106:109], v[180:183], v[188:191], v[106:109]
	v_mfma_f32_16x16x32_bf16 v[98:101], v[172:175], v[196:199], v[98:101]
	v_mfma_f32_16x16x32_bf16 v[90:93], v[180:183], v[196:199], v[90:93]
	v_mfma_f32_16x16x32_bf16 v[82:85], v[172:175], v[204:207], v[82:85]
	v_mfma_f32_16x16x32_bf16 v[74:77], v[180:183], v[204:207], v[74:77]
	v_mfma_f32_16x16x32_bf16 v[70:73], v[172:175], v[212:215], v[70:73]
	v_mfma_f32_16x16x32_bf16 v[66:69], v[180:183], v[212:215], v[66:69]
	s_setprio 0
	s_barrier
	s_add_i32 s70, s61, s33
	s_mov_b32 m0, s70
	ds_read_b128 v[184:187], v154 offset:16384
	ds_read_b128 v[188:191], v154 offset:17408
	ds_read_b128 v[192:195], v154 offset:18432
	ds_read_b128 v[196:199], v154 offset:19456
	ds_read_b128 v[200:203], v154 offset:20480
	ds_read_b128 v[204:207], v154 offset:21504
	ds_read_b128 v[208:211], v154 offset:22528
	ds_read_b128 v[212:215], v154 offset:23552
	global_load_lds_dwordx4 v134, s[24:25]
	s_add_i32 m0, s70, 0x2000
	s_add_u32 s70, s24, 0x80000
	s_addc_u32 s71, s25, 0
	s_add_i32 s72, s62, s33
	global_load_lds_dwordx4 v130, s[24:25]
	s_mov_b32 m0, s72
	s_nop 0
	global_load_lds_dwordx4 v134, s[70:71]
	s_add_i32 m0, s72, 0x2000
	s_nop 0
	global_load_lds_dwordx4 v130, s[70:71]
	s_mov_b32 m0, s21
	s_nop 0
	global_load_lds_dwordx4 v136, s[26:27]
	s_mov_b32 m0, s36
	s_nop 0
	global_load_lds_dwordx4 v132, s[26:27]
	s_add_u32 s98, s24, 0x80
	s_addc_u32 s99, s25, 0
	s_add_u32 s100, s26, 0x80
	s_addc_u32 s101, s27, 0
	s_waitcnt vmcnt(8)
	s_waitcnt lgkmcnt(0)
	s_barrier
	s_setprio 1
	s_waitcnt lgkmcnt(0)
	v_mfma_f32_16x16x32_bf16 v[62:65], v[146:149], v[184:187], v[62:65]
	v_mfma_f32_16x16x32_bf16 v[58:61], v[160:163], v[184:187], v[58:61]
	v_mfma_f32_16x16x32_bf16 v[54:57], v[146:149], v[192:195], v[54:57]
	v_mfma_f32_16x16x32_bf16 v[46:49], v[160:163], v[192:195], v[46:49]
	v_mfma_f32_16x16x32_bf16 v[38:41], v[146:149], v[200:203], v[38:41]
	v_mfma_f32_16x16x32_bf16 v[30:33], v[160:163], v[200:203], v[30:33]
	v_mfma_f32_16x16x32_bf16 v[22:25], v[146:149], v[208:211], v[22:25]
	v_mfma_f32_16x16x32_bf16 v[14:17], v[160:163], v[208:211], v[14:17]
	v_mfma_f32_16x16x32_bf16 v[62:65], v[156:159], v[188:191], v[62:65]
	v_mfma_f32_16x16x32_bf16 v[58:61], v[164:167], v[188:191], v[58:61]
	v_mfma_f32_16x16x32_bf16 v[54:57], v[156:159], v[196:199], v[54:57]
	v_mfma_f32_16x16x32_bf16 v[46:49], v[164:167], v[196:199], v[46:49]
	v_mfma_f32_16x16x32_bf16 v[38:41], v[156:159], v[204:207], v[38:41]
	v_mfma_f32_16x16x32_bf16 v[30:33], v[164:167], v[204:207], v[30:33]
	v_mfma_f32_16x16x32_bf16 v[22:25], v[156:159], v[212:215], v[22:25]
	v_mfma_f32_16x16x32_bf16 v[14:17], v[164:167], v[212:215], v[14:17]
	s_setprio 0
	s_setprio 1
	v_mfma_f32_16x16x32_bf16 v[50:53], v[168:171], v[184:187], v[50:53]
	v_mfma_f32_16x16x32_bf16 v[42:45], v[176:179], v[184:187], v[42:45]
	v_mfma_f32_16x16x32_bf16 v[34:37], v[168:171], v[192:195], v[34:37]
	v_mfma_f32_16x16x32_bf16 v[26:29], v[176:179], v[192:195], v[26:29]
	v_mfma_f32_16x16x32_bf16 v[18:21], v[168:171], v[200:203], v[18:21]
	v_mfma_f32_16x16x32_bf16 v[10:13], v[176:179], v[200:203], v[10:13]
	v_mfma_f32_16x16x32_bf16 v[6:9], v[168:171], v[208:211], v[6:9]
	v_mfma_f32_16x16x32_bf16 v[2:5], v[176:179], v[208:211], v[2:5]
	v_mfma_f32_16x16x32_bf16 v[50:53], v[172:175], v[188:191], v[50:53]
	v_mfma_f32_16x16x32_bf16 v[42:45], v[180:183], v[188:191], v[42:45]
	v_mfma_f32_16x16x32_bf16 v[34:37], v[172:175], v[196:199], v[34:37]
	v_mfma_f32_16x16x32_bf16 v[26:29], v[180:183], v[196:199], v[26:29]
	v_mfma_f32_16x16x32_bf16 v[18:21], v[172:175], v[204:207], v[18:21]
	v_mfma_f32_16x16x32_bf16 v[10:13], v[180:183], v[204:207], v[10:13]
	v_mfma_f32_16x16x32_bf16 v[6:9], v[172:175], v[212:215], v[6:9]
	v_mfma_f32_16x16x32_bf16 v[2:5], v[180:183], v[212:215], v[2:5]
	s_setprio 0
	s_barrier
	s_add_i32 s70, 0, 0x18000
	v_add_u32_e32 v155, s70, v150
	s_add_i32 s71, 0, 0x1c000
	ds_read_b128 v[146:149], v155
	ds_read_b128 v[156:159], v155 offset:1024
	ds_read_b128 v[160:163], v155 offset:2048
	ds_read_b128 v[164:167], v155 offset:3072
	v_add_u32_e32 v155, s71, v150
	ds_read_b128 v[168:171], v155
	ds_read_b128 v[172:175], v155 offset:1024
	ds_read_b128 v[176:179], v155 offset:2048
	ds_read_b128 v[180:183], v155 offset:3072
	s_add_u32 s26, s26, 0x80000
	s_addc_u32 s27, s27, 0
	s_mov_b32 m0, s37
	ds_read_b128 v[184:187], v154 offset:32768
	ds_read_b128 v[188:191], v154 offset:33792
	ds_read_b128 v[192:195], v154 offset:34816
	ds_read_b128 v[196:199], v154 offset:35840
	ds_read_b128 v[200:203], v154 offset:36864
	ds_read_b128 v[204:207], v154 offset:37888
	ds_read_b128 v[208:211], v154 offset:38912
	ds_read_b128 v[212:215], v154 offset:39936
	global_load_lds_dwordx4 v136, s[26:27]
	s_mov_b32 m0, s42
	s_nop 0
	global_load_lds_dwordx4 v132, s[26:27]
	s_waitcnt vmcnt(8)
	s_waitcnt lgkmcnt(0)
	s_barrier
	s_setprio 1
	s_waitcnt lgkmcnt(0)
	v_mfma_f32_16x16x32_bf16 v[126:129], v[146:149], v[184:187], v[126:129]
	v_mfma_f32_16x16x32_bf16 v[122:125], v[160:163], v[184:187], v[122:125]
	v_mfma_f32_16x16x32_bf16 v[118:121], v[146:149], v[192:195], v[118:121]
	v_mfma_f32_16x16x32_bf16 v[110:113], v[160:163], v[192:195], v[110:113]
	v_mfma_f32_16x16x32_bf16 v[102:105], v[146:149], v[200:203], v[102:105]
	v_mfma_f32_16x16x32_bf16 v[94:97], v[160:163], v[200:203], v[94:97]
	v_mfma_f32_16x16x32_bf16 v[86:89], v[146:149], v[208:211], v[86:89]
	v_mfma_f32_16x16x32_bf16 v[78:81], v[160:163], v[208:211], v[78:81]
	v_mfma_f32_16x16x32_bf16 v[126:129], v[156:159], v[188:191], v[126:129]
	v_mfma_f32_16x16x32_bf16 v[122:125], v[164:167], v[188:191], v[122:125]
	v_mfma_f32_16x16x32_bf16 v[118:121], v[156:159], v[196:199], v[118:121]
	v_mfma_f32_16x16x32_bf16 v[110:113], v[164:167], v[196:199], v[110:113]
	v_mfma_f32_16x16x32_bf16 v[102:105], v[156:159], v[204:207], v[102:105]
	v_mfma_f32_16x16x32_bf16 v[94:97], v[164:167], v[204:207], v[94:97]
	v_mfma_f32_16x16x32_bf16 v[86:89], v[156:159], v[212:215], v[86:89]
	v_mfma_f32_16x16x32_bf16 v[78:81], v[164:167], v[212:215], v[78:81]
	s_setprio 0
	s_setprio 1
	v_mfma_f32_16x16x32_bf16 v[114:117], v[168:171], v[184:187], v[114:117]
	v_mfma_f32_16x16x32_bf16 v[106:109], v[176:179], v[184:187], v[106:109]
	v_mfma_f32_16x16x32_bf16 v[98:101], v[168:171], v[192:195], v[98:101]
	v_mfma_f32_16x16x32_bf16 v[90:93], v[176:179], v[192:195], v[90:93]
	v_mfma_f32_16x16x32_bf16 v[82:85], v[168:171], v[200:203], v[82:85]
	v_mfma_f32_16x16x32_bf16 v[74:77], v[176:179], v[200:203], v[74:77]
	v_mfma_f32_16x16x32_bf16 v[70:73], v[168:171], v[208:211], v[70:73]
	v_mfma_f32_16x16x32_bf16 v[66:69], v[176:179], v[208:211], v[66:69]
	v_mfma_f32_16x16x32_bf16 v[114:117], v[172:175], v[188:191], v[114:117]
	v_mfma_f32_16x16x32_bf16 v[106:109], v[180:183], v[188:191], v[106:109]
	v_mfma_f32_16x16x32_bf16 v[98:101], v[172:175], v[196:199], v[98:101]
	v_mfma_f32_16x16x32_bf16 v[90:93], v[180:183], v[196:199], v[90:93]
	v_mfma_f32_16x16x32_bf16 v[82:85], v[172:175], v[204:207], v[82:85]
	v_mfma_f32_16x16x32_bf16 v[74:77], v[180:183], v[204:207], v[74:77]
	v_mfma_f32_16x16x32_bf16 v[70:73], v[172:175], v[212:215], v[70:73]
	v_mfma_f32_16x16x32_bf16 v[66:69], v[180:183], v[212:215], v[66:69]
	s_setprio 0
	s_barrier
	s_add_i32 s26, s70, s33
	s_mov_b32 m0, s26
	ds_read_b128 v[184:187], v154 offset:49152
	ds_read_b128 v[188:191], v154 offset:50176
	ds_read_b128 v[192:195], v154 offset:51200
	ds_read_b128 v[196:199], v154 offset:52224
	ds_read_b128 v[200:203], v154 offset:53248
	ds_read_b128 v[204:207], v154 offset:54272
	ds_read_b128 v[208:211], v154 offset:55296
	ds_read_b128 v[212:215], v154 offset:56320
	global_load_lds_dwordx4 v134, s[98:99]
	s_add_i32 m0, s26, 0x2000
	s_add_u32 s24, s24, 0x80080
	s_addc_u32 s25, s25, 0
	s_add_i32 s26, s71, s33
	global_load_lds_dwordx4 v130, s[98:99]
	s_mov_b32 m0, s26
	s_nop 0
	global_load_lds_dwordx4 v134, s[24:25]
	s_add_i32 m0, s26, 0x2000
	s_nop 0
	global_load_lds_dwordx4 v130, s[24:25]
	s_mov_b32 m0, s44
	s_nop 0
	global_load_lds_dwordx4 v136, s[100:101]
	s_mov_b32 m0, s45
	s_nop 0
	global_load_lds_dwordx4 v132, s[100:101]
	s_waitcnt vmcnt(8)
	s_waitcnt lgkmcnt(0)
	s_barrier
	s_setprio 1
	s_waitcnt lgkmcnt(0)
	v_mfma_f32_16x16x32_bf16 v[62:65], v[146:149], v[184:187], v[62:65]
	v_mfma_f32_16x16x32_bf16 v[58:61], v[160:163], v[184:187], v[58:61]
	v_mfma_f32_16x16x32_bf16 v[54:57], v[146:149], v[192:195], v[54:57]
	v_mfma_f32_16x16x32_bf16 v[46:49], v[160:163], v[192:195], v[46:49]
	v_mfma_f32_16x16x32_bf16 v[38:41], v[146:149], v[200:203], v[38:41]
	v_mfma_f32_16x16x32_bf16 v[30:33], v[160:163], v[200:203], v[30:33]
	v_mfma_f32_16x16x32_bf16 v[22:25], v[146:149], v[208:211], v[22:25]
	v_mfma_f32_16x16x32_bf16 v[14:17], v[160:163], v[208:211], v[14:17]
	v_mfma_f32_16x16x32_bf16 v[62:65], v[156:159], v[188:191], v[62:65]
	v_mfma_f32_16x16x32_bf16 v[58:61], v[164:167], v[188:191], v[58:61]
	v_mfma_f32_16x16x32_bf16 v[54:57], v[156:159], v[196:199], v[54:57]
	v_mfma_f32_16x16x32_bf16 v[46:49], v[164:167], v[196:199], v[46:49]
	v_mfma_f32_16x16x32_bf16 v[38:41], v[156:159], v[204:207], v[38:41]
	v_mfma_f32_16x16x32_bf16 v[30:33], v[164:167], v[204:207], v[30:33]
	v_mfma_f32_16x16x32_bf16 v[22:25], v[156:159], v[212:215], v[22:25]
	v_mfma_f32_16x16x32_bf16 v[14:17], v[164:167], v[212:215], v[14:17]
	s_setprio 0
	s_setprio 1
	v_mfma_f32_16x16x32_bf16 v[50:53], v[168:171], v[184:187], v[50:53]
	v_mfma_f32_16x16x32_bf16 v[42:45], v[176:179], v[184:187], v[42:45]
	v_mfma_f32_16x16x32_bf16 v[34:37], v[168:171], v[192:195], v[34:37]
	v_mfma_f32_16x16x32_bf16 v[26:29], v[176:179], v[192:195], v[26:29]
	v_mfma_f32_16x16x32_bf16 v[18:21], v[168:171], v[200:203], v[18:21]
	v_mfma_f32_16x16x32_bf16 v[10:13], v[176:179], v[200:203], v[10:13]
	v_mfma_f32_16x16x32_bf16 v[6:9], v[168:171], v[208:211], v[6:9]
	v_mfma_f32_16x16x32_bf16 v[2:5], v[176:179], v[208:211], v[2:5]
	v_mfma_f32_16x16x32_bf16 v[50:53], v[172:175], v[188:191], v[50:53]
	v_mfma_f32_16x16x32_bf16 v[42:45], v[180:183], v[188:191], v[42:45]
	v_mfma_f32_16x16x32_bf16 v[34:37], v[172:175], v[196:199], v[34:37]
	v_mfma_f32_16x16x32_bf16 v[26:29], v[180:183], v[196:199], v[26:29]
	v_mfma_f32_16x16x32_bf16 v[18:21], v[172:175], v[204:207], v[18:21]
	v_mfma_f32_16x16x32_bf16 v[10:13], v[180:183], v[204:207], v[10:13]
	v_mfma_f32_16x16x32_bf16 v[6:9], v[172:175], v[212:215], v[6:9]
	v_mfma_f32_16x16x32_bf16 v[2:5], v[180:183], v[212:215], v[2:5]
	s_setprio 0
	s_barrier
	s_add_i32 s69, s69, 2
	s_add_u32 s22, s22, 0x100
	s_addc_u32 s23, s23, 0
	s_add_u32 s67, s67, 0x100
	s_addc_u32 s68, s68, 0
	s_cmp_gt_u32 s69, 29
	s_cbranch_scc0 .LBB0_767
	s_nop 0
	s_nop 0
	s_nop 0
	s_nop 0
	s_nop 0
	s_nop 0
	s_nop 0
	s_nop 0
	s_nop 0
	s_and_b64 vcc, exec, s[10:11]
	s_cbranch_vccz .LBB0_770
	s_barrier

.LBB0_1043:
	ds_read_b128 v[26:29], v209
	ds_read_b128 v[30:33], v209 offset:1024
	ds_read_b128 v[18:21], v209 offset:2048
	ds_read_b128 v[22:25], v209 offset:3072
	ds_read_b128 v[10:13], v210
	ds_read_b128 v[14:17], v210 offset:1024
	ds_read_b128 v[2:5], v210 offset:2048
	ds_read_b128 v[6:9], v210 offset:3072
	s_add_u32 s44, s40, 0xfffc0080
	s_addc_u32 s45, s41, -1
	s_cmp_eq_u32 s81, 12
	s_cselect_b32 s49, s1, s45
	s_cselect_b32 s48, s35, s44
	s_cselect_b32 s45, s31, s61
	s_cselect_b32 s44, s43, s60
	s_add_i32 m0, s65, 0xc000
	ds_read_b128 v[182:185], v211
	ds_read_b128 v[186:189], v211 offset:1024
	ds_read_b128 v[190:193], v211 offset:2048
	ds_read_b128 v[194:197], v211 offset:3072
	ds_read_b128 v[218:221], v211 offset:4096
	ds_read_b128 v[222:225], v211 offset:5120
	ds_read_b128 v[226:229], v211 offset:6144
	ds_read_b128 v[230:233], v211 offset:7168
	global_load_lds_dwordx4 v174, s[40:41]
	s_add_i32 m0, s65, 0xe000
	s_nop 0
	global_load_lds_dwordx4 v176, s[40:41]
	s_waitcnt vmcnt(8)
	s_waitcnt lgkmcnt(0)
	s_barrier
	s_setprio 1
	s_waitcnt lgkmcnt(0)
	v_mfma_scale_f32_16x16x128_f8f6f4 v[158:161], v[26:33], v[182:189], v[158:161], v212, v213 op_sel_hi:[0,0,0]
	v_mfma_scale_f32_16x16x128_f8f6f4 v[154:157], v[18:25], v[182:189], v[154:157], v212, v213 op_sel_hi:[0,0,0]
	v_mfma_scale_f32_16x16x128_f8f6f4 v[142:145], v[26:33], v[190:197], v[142:145], v212, v213 op_sel_hi:[0,0,0]
	v_mfma_scale_f32_16x16x128_f8f6f4 v[138:141], v[18:25], v[190:197], v[138:141], v212, v213 op_sel_hi:[0,0,0]
	v_mfma_scale_f32_16x16x128_f8f6f4 v[126:129], v[26:33], v[218:225], v[126:129], v212, v213 op_sel_hi:[0,0,0]
	v_mfma_scale_f32_16x16x128_f8f6f4 v[122:125], v[18:25], v[218:225], v[122:125], v212, v213 op_sel_hi:[0,0,0]
	v_mfma_scale_f32_16x16x128_f8f6f4 v[110:113], v[26:33], v[226:233], v[110:113], v212, v213 op_sel_hi:[0,0,0]
	v_mfma_scale_f32_16x16x128_f8f6f4 v[106:109], v[18:25], v[226:233], v[106:109], v212, v213 op_sel_hi:[0,0,0]
	s_setprio 0
	s_setprio 1
	v_mfma_scale_f32_16x16x128_f8f6f4 v[150:153], v[10:17], v[182:189], v[150:153], v212, v213 op_sel_hi:[0,0,0]
	v_mfma_scale_f32_16x16x128_f8f6f4 v[146:149], v[2:9], v[182:189], v[146:149], v212, v213 op_sel_hi:[0,0,0]
	v_mfma_scale_f32_16x16x128_f8f6f4 v[134:137], v[10:17], v[190:197], v[134:137], v212, v213 op_sel_hi:[0,0,0]
	v_mfma_scale_f32_16x16x128_f8f6f4 v[130:133], v[2:9], v[190:197], v[130:133], v212, v213 op_sel_hi:[0,0,0]
	v_mfma_scale_f32_16x16x128_f8f6f4 v[118:121], v[10:17], v[218:225], v[118:121], v212, v213 op_sel_hi:[0,0,0]
	v_mfma_scale_f32_16x16x128_f8f6f4 v[114:117], v[2:9], v[218:225], v[114:117], v212, v213 op_sel_hi:[0,0,0]
	v_mfma_scale_f32_16x16x128_f8f6f4 v[102:105], v[10:17], v[226:233], v[102:105], v212, v213 op_sel_hi:[0,0,0]
	v_mfma_scale_f32_16x16x128_f8f6f4 v[98:101], v[2:9], v[226:233], v[98:101], v212, v213 op_sel_hi:[0,0,0]
	s_setprio 0
	s_barrier
	s_add_i32 s82, s77, s64
	s_mov_b32 m0, s82
	ds_read_b128 v[190:193], v211 offset:16384
	ds_read_b128 v[194:197], v211 offset:17408
	ds_read_b128 v[218:221], v211 offset:18432
	ds_read_b128 v[222:225], v211 offset:19456
	ds_read_b128 v[226:229], v211 offset:20480
	ds_read_b128 v[230:233], v211 offset:21504
	ds_read_b128 v[234:237], v211 offset:22528
	ds_read_b128 v[238:241], v211 offset:23552
	global_load_lds_dwordx4 v164, s[44:45]
	s_add_i32 m0, s82, 0x2000
	s_add_u32 s82, s44, 0x40000
	s_addc_u32 s83, s45, 0
	s_add_i32 s84, s78, s64
	global_load_lds_dwordx4 v168, s[44:45]
	s_mov_b32 m0, s84
	s_nop 0
	global_load_lds_dwordx4 v164, s[82:83]
	s_add_i32 m0, s84, 0x2000
	s_nop 0
	global_load_lds_dwordx4 v168, s[82:83]
	s_mov_b32 m0, s65
	s_nop 0
	global_load_lds_dwordx4 v162, s[48:49]
	s_mov_b32 m0, s66
	s_nop 0
	global_load_lds_dwordx4 v166, s[48:49]
	s_add_u32 s98, s44, 0x80
	s_addc_u32 s99, s45, 0
	s_add_u32 s100, s48, 0x80
	s_addc_u32 s101, s49, 0
	s_waitcnt vmcnt(8)
	s_waitcnt lgkmcnt(0)
	s_barrier
	s_setprio 1
	s_waitcnt lgkmcnt(0)
	v_mfma_scale_f32_16x16x128_f8f6f4 v[94:97], v[26:33], v[190:197], v[94:97], v212, v213 op_sel_hi:[0,0,0]
	v_mfma_scale_f32_16x16x128_f8f6f4 v[90:93], v[18:25], v[190:197], v[90:93], v212, v213 op_sel_hi:[0,0,0]
	v_mfma_scale_f32_16x16x128_f8f6f4 v[78:81], v[26:33], v[218:225], v[78:81], v212, v213 op_sel_hi:[0,0,0]
	v_mfma_scale_f32_16x16x128_f8f6f4 v[74:77], v[18:25], v[218:225], v[74:77], v212, v213 op_sel_hi:[0,0,0]
	v_mfma_scale_f32_16x16x128_f8f6f4 v[62:65], v[26:33], v[226:233], v[62:65], v212, v213 op_sel_hi:[0,0,0]
	v_mfma_scale_f32_16x16x128_f8f6f4 v[58:61], v[18:25], v[226:233], v[58:61], v212, v213 op_sel_hi:[0,0,0]
	v_mfma_scale_f32_16x16x128_f8f6f4 v[46:49], v[26:33], v[234:241], v[46:49], v212, v213 op_sel_hi:[0,0,0]
	v_mfma_scale_f32_16x16x128_f8f6f4 v[42:45], v[18:25], v[234:241], v[42:45], v212, v213 op_sel_hi:[0,0,0]
	s_setprio 0
	s_setprio 1
	v_mfma_scale_f32_16x16x128_f8f6f4 v[86:89], v[10:17], v[190:197], v[86:89], v212, v213 op_sel_hi:[0,0,0]
	v_mfma_scale_f32_16x16x128_f8f6f4 v[82:85], v[2:9], v[190:197], v[82:85], v212, v213 op_sel_hi:[0,0,0]
	v_mfma_scale_f32_16x16x128_f8f6f4 v[70:73], v[10:17], v[218:225], v[70:73], v212, v213 op_sel_hi:[0,0,0]
	v_mfma_scale_f32_16x16x128_f8f6f4 v[66:69], v[2:9], v[218:225], v[66:69], v212, v213 op_sel_hi:[0,0,0]
	v_mfma_scale_f32_16x16x128_f8f6f4 v[54:57], v[10:17], v[226:233], v[54:57], v212, v213 op_sel_hi:[0,0,0]
	v_mfma_scale_f32_16x16x128_f8f6f4 v[50:53], v[2:9], v[226:233], v[50:53], v212, v213 op_sel_hi:[0,0,0]
	v_mfma_scale_f32_16x16x128_f8f6f4 v[38:41], v[10:17], v[234:241], v[38:41], v212, v213 op_sel_hi:[0,0,0]
	v_mfma_scale_f32_16x16x128_f8f6f4 v[34:37], v[2:9], v[234:241], v[34:37], v212, v213 op_sel_hi:[0,0,0]
	s_setprio 0
	s_barrier
	s_add_i32 s82, 0, 0x18000
	s_add_i32 s83, 0, 0x1c000
	v_add_u32_e32 v14, s82, v202
	v_add_u32_e32 v30, s83, v202
	ds_read_b128 v[2:5], v14
	ds_read_b128 v[6:9], v14 offset:1024
	ds_read_b128 v[10:13], v14 offset:2048
	ds_read_b128 v[14:17], v14 offset:3072
	ds_read_b128 v[18:21], v30
	ds_read_b128 v[22:25], v30 offset:1024
	ds_read_b128 v[26:29], v30 offset:2048
	ds_read_b128 v[30:33], v30 offset:3072
	s_add_u32 s48, s48, 0x40000
	s_addc_u32 s49, s49, 0
	s_mov_b32 m0, s67
	ds_read_b128 v[190:193], v211 offset:32768
	ds_read_b128 v[194:197], v211 offset:33792
	ds_read_b128 v[218:221], v211 offset:34816
	ds_read_b128 v[222:225], v211 offset:35840
	ds_read_b128 v[226:229], v211 offset:36864
	ds_read_b128 v[230:233], v211 offset:37888
	ds_read_b128 v[234:237], v211 offset:38912
	ds_read_b128 v[238:241], v211 offset:39936
	global_load_lds_dwordx4 v162, s[48:49]
	s_mov_b32 m0, s68
	s_nop 0
	global_load_lds_dwordx4 v166, s[48:49]
	s_waitcnt vmcnt(8)
	s_waitcnt lgkmcnt(0)
	s_barrier
	s_setprio 1
	s_waitcnt lgkmcnt(0)
	v_mfma_scale_f32_16x16x128_f8f6f4 v[158:161], v[2:9], v[190:197], v[158:161], v212, v213 op_sel_hi:[0,0,0]
	v_mfma_scale_f32_16x16x128_f8f6f4 v[154:157], v[10:17], v[190:197], v[154:157], v212, v213 op_sel_hi:[0,0,0]
	v_mfma_scale_f32_16x16x128_f8f6f4 v[142:145], v[2:9], v[218:225], v[142:145], v212, v213 op_sel_hi:[0,0,0]
	v_mfma_scale_f32_16x16x128_f8f6f4 v[138:141], v[10:17], v[218:225], v[138:141], v212, v213 op_sel_hi:[0,0,0]
	v_mfma_scale_f32_16x16x128_f8f6f4 v[126:129], v[2:9], v[226:233], v[126:129], v212, v213 op_sel_hi:[0,0,0]
	v_mfma_scale_f32_16x16x128_f8f6f4 v[122:125], v[10:17], v[226:233], v[122:125], v212, v213 op_sel_hi:[0,0,0]
	v_mfma_scale_f32_16x16x128_f8f6f4 v[110:113], v[2:9], v[234:241], v[110:113], v212, v213 op_sel_hi:[0,0,0]
	v_mfma_scale_f32_16x16x128_f8f6f4 v[106:109], v[10:17], v[234:241], v[106:109], v212, v213 op_sel_hi:[0,0,0]
	s_setprio 0
	s_setprio 1
	v_mfma_scale_f32_16x16x128_f8f6f4 v[150:153], v[18:25], v[190:197], v[150:153], v212, v213 op_sel_hi:[0,0,0]
	v_mfma_scale_f32_16x16x128_f8f6f4 v[146:149], v[26:33], v[190:197], v[146:149], v212, v213 op_sel_hi:[0,0,0]
	v_mfma_scale_f32_16x16x128_f8f6f4 v[134:137], v[18:25], v[218:225], v[134:137], v212, v213 op_sel_hi:[0,0,0]
	v_mfma_scale_f32_16x16x128_f8f6f4 v[130:133], v[26:33], v[218:225], v[130:133], v212, v213 op_sel_hi:[0,0,0]
	v_mfma_scale_f32_16x16x128_f8f6f4 v[118:121], v[18:25], v[226:233], v[118:121], v212, v213 op_sel_hi:[0,0,0]
	v_mfma_scale_f32_16x16x128_f8f6f4 v[114:117], v[26:33], v[226:233], v[114:117], v212, v213 op_sel_hi:[0,0,0]
	v_mfma_scale_f32_16x16x128_f8f6f4 v[102:105], v[18:25], v[234:241], v[102:105], v212, v213 op_sel_hi:[0,0,0]
	v_mfma_scale_f32_16x16x128_f8f6f4 v[98:101], v[26:33], v[234:241], v[98:101], v212, v213 op_sel_hi:[0,0,0]
	s_setprio 0
	s_barrier
	s_add_i32 s48, s82, s64
	s_mov_b32 m0, s48
	ds_read_b128 v[190:193], v211 offset:49152
	ds_read_b128 v[194:197], v211 offset:50176
	ds_read_b128 v[218:221], v211 offset:51200
	ds_read_b128 v[222:225], v211 offset:52224
	ds_read_b128 v[226:229], v211 offset:53248
	ds_read_b128 v[230:233], v211 offset:54272
	ds_read_b128 v[234:237], v211 offset:55296
	ds_read_b128 v[238:241], v211 offset:56320
	global_load_lds_dwordx4 v164, s[98:99]
	s_add_i32 m0, s48, 0x2000
	s_add_u32 s44, s44, 0x40080
	s_addc_u32 s45, s45, 0
	s_add_i32 s48, s83, s64
	global_load_lds_dwordx4 v168, s[98:99]
	s_mov_b32 m0, s48
	s_nop 0
	global_load_lds_dwordx4 v164, s[44:45]
	s_add_i32 m0, s48, 0x2000
	s_nop 0
	global_load_lds_dwordx4 v168, s[44:45]
	s_mov_b32 m0, s72
	s_nop 0
	global_load_lds_dwordx4 v162, s[100:101]
	s_mov_b32 m0, s73
	s_nop 0
	global_load_lds_dwordx4 v166, s[100:101]
	s_waitcnt vmcnt(8)
	s_waitcnt lgkmcnt(0)
	s_barrier
	s_setprio 1
	s_waitcnt lgkmcnt(0)
	v_mfma_scale_f32_16x16x128_f8f6f4 v[94:97], v[2:9], v[190:197], v[94:97], v212, v213 op_sel_hi:[0,0,0]
	v_mfma_scale_f32_16x16x128_f8f6f4 v[90:93], v[10:17], v[190:197], v[90:93], v212, v213 op_sel_hi:[0,0,0]
	v_mfma_scale_f32_16x16x128_f8f6f4 v[78:81], v[2:9], v[218:225], v[78:81], v212, v213 op_sel_hi:[0,0,0]
	v_mfma_scale_f32_16x16x128_f8f6f4 v[74:77], v[10:17], v[218:225], v[74:77], v212, v213 op_sel_hi:[0,0,0]
	v_mfma_scale_f32_16x16x128_f8f6f4 v[62:65], v[2:9], v[226:233], v[62:65], v212, v213 op_sel_hi:[0,0,0]
	v_mfma_scale_f32_16x16x128_f8f6f4 v[58:61], v[10:17], v[226:233], v[58:61], v212, v213 op_sel_hi:[0,0,0]
	v_mfma_scale_f32_16x16x128_f8f6f4 v[46:49], v[2:9], v[234:241], v[46:49], v212, v213 op_sel_hi:[0,0,0]
	v_mfma_scale_f32_16x16x128_f8f6f4 v[42:45], v[10:17], v[234:241], v[42:45], v212, v213 op_sel_hi:[0,0,0]
	s_setprio 0
	s_setprio 1
	v_mfma_scale_f32_16x16x128_f8f6f4 v[86:89], v[18:25], v[190:197], v[86:89], v212, v213 op_sel_hi:[0,0,0]
	v_mfma_scale_f32_16x16x128_f8f6f4 v[82:85], v[26:33], v[190:197], v[82:85], v212, v213 op_sel_hi:[0,0,0]
	v_mfma_scale_f32_16x16x128_f8f6f4 v[70:73], v[18:25], v[218:225], v[70:73], v212, v213 op_sel_hi:[0,0,0]
	v_mfma_scale_f32_16x16x128_f8f6f4 v[66:69], v[26:33], v[218:225], v[66:69], v212, v213 op_sel_hi:[0,0,0]
	v_mfma_scale_f32_16x16x128_f8f6f4 v[54:57], v[18:25], v[226:233], v[54:57], v212, v213 op_sel_hi:[0,0,0]
	v_mfma_scale_f32_16x16x128_f8f6f4 v[50:53], v[26:33], v[226:233], v[50:53], v212, v213 op_sel_hi:[0,0,0]
	v_mfma_scale_f32_16x16x128_f8f6f4 v[38:41], v[18:25], v[234:241], v[38:41], v212, v213 op_sel_hi:[0,0,0]
	v_mfma_scale_f32_16x16x128_f8f6f4 v[34:37], v[26:33], v[234:241], v[34:37], v212, v213 op_sel_hi:[0,0,0]
	s_setprio 0
	s_barrier
	s_add_i32 s81, s81, 2
	s_add_u32 s40, s40, 0x100
	s_addc_u32 s41, s41, 0
	s_add_u32 s60, s60, 0x100
	s_addc_u32 s61, s61, 0
	s_cmp_gt_u32 s81, 13
	s_cbranch_scc0 .LBB0_1043
	s_nop 0
	s_nop 0
	s_nop 0
	s_nop 0
	s_nop 0
	s_nop 0
	s_nop 0
	s_nop 0
	s_nop 0
	s_and_b64 vcc, exec, s[26:27]
	s_cbranch_vccz .LBB0_1046
	s_barrier

.LBB0_1257:
	ds_read_b128 v[20:23], v202
	ds_read_b128 v[166:169], v202 offset:1024
	ds_read_b128 v[14:17], v202 offset:2048
	ds_read_b128 v[162:165], v202 offset:3072
	ds_read_b128 v[8:11], v203
	ds_read_b128 v[158:161], v203 offset:1024
	ds_read_b128 v[2:5], v203 offset:2048
	ds_read_b128 v[154:157], v203 offset:3072
	s_add_u32 s22, s20, 0xfffc0080
	s_addc_u32 s23, s21, -1
	s_cmp_eq_u32 s63, 12
	s_cselect_b32 s25, s11, s23
	s_cselect_b32 s24, s49, s22
	s_cselect_b32 s23, s13, s62
	s_cselect_b32 s22, s60, s61
	s_add_i32 m0, s35, 0xc000
	ds_read_b128 v[184:187], v204
	ds_read_b128 v[188:191], v204 offset:1024
	ds_read_b128 v[206:209], v204 offset:2048
	ds_read_b128 v[222:225], v204 offset:3072
	ds_read_b128 v[212:215], v204 offset:4096
	ds_read_b128 v[226:229], v204 offset:5120
	ds_read_b128 v[218:221], v204 offset:6144
	ds_read_b128 v[230:233], v204 offset:7168
	global_load_lds_dwordx4 v180, s[20:21]
	s_add_i32 m0, s35, 0xe000
	s_nop 0
	global_load_lds_dwordx4 v182, s[20:21]
	s_waitcnt vmcnt(8)
	s_waitcnt lgkmcnt(0)
	s_barrier
	s_setprio 1
	s_waitcnt lgkmcnt(0)
	v_mov_b32_e32 v24, v166
	v_mov_b32_e32 v25, v167
	s_nop 1
	v_mfma_scale_f32_16x16x128_f8f6f4 v[150:153], v[20:25], v[184:189], v[150:153], v168, v190 op_sel_hi:[0,0,0] cbsz:2 blgp:2
	v_mov_b32_e32 v18, v162
	v_mov_b32_e32 v19, v163
	s_nop 1
	v_mfma_scale_f32_16x16x128_f8f6f4 v[138:141], v[14:19], v[184:189], v[138:141], v164, v190 op_sel_hi:[0,0,0] cbsz:2 blgp:2
	v_mov_b32_e32 v210, v222
	v_mov_b32_e32 v211, v223
	s_nop 1
	v_mfma_scale_f32_16x16x128_f8f6f4 v[134:137], v[20:25], v[206:211], v[134:137], v168, v224 op_sel_hi:[0,0,0] cbsz:2 blgp:2
	v_mfma_scale_f32_16x16x128_f8f6f4 v[122:125], v[14:19], v[206:211], v[122:125], v164, v224 op_sel_hi:[0,0,0] cbsz:2 blgp:2
	v_mov_b32_e32 v216, v226
	v_mov_b32_e32 v217, v227
	s_nop 1
	v_mfma_scale_f32_16x16x128_f8f6f4 v[118:121], v[20:25], v[212:217], v[118:121], v168, v228 op_sel_hi:[0,0,0] cbsz:2 blgp:2
	v_mfma_scale_f32_16x16x128_f8f6f4 v[106:109], v[14:19], v[212:217], v[106:109], v164, v228 op_sel_hi:[0,0,0] cbsz:2 blgp:2
	v_mov_b32_e32 v222, v230
	v_mov_b32_e32 v223, v231
	s_nop 1
	v_mfma_scale_f32_16x16x128_f8f6f4 v[102:105], v[20:25], v[218:223], v[102:105], v168, v232 op_sel_hi:[0,0,0] cbsz:2 blgp:2
	v_mfma_scale_f32_16x16x128_f8f6f4 v[90:93], v[14:19], v[218:223], v[90:93], v164, v232 op_sel_hi:[0,0,0] cbsz:2 blgp:2
	s_setprio 0
	s_setprio 1
	v_mov_b32_e32 v12, v158
	v_mov_b32_e32 v13, v159
	s_nop 1
	v_mfma_scale_f32_16x16x128_f8f6f4 v[146:149], v[8:13], v[184:189], v[146:149], v160, v190 op_sel_hi:[0,0,0] cbsz:2 blgp:2
	v_mov_b32_e32 v6, v154
	v_mov_b32_e32 v7, v155
	s_nop 1
	v_mfma_scale_f32_16x16x128_f8f6f4 v[142:145], v[2:7], v[184:189], v[142:145], v156, v190 op_sel_hi:[0,0,0] cbsz:2 blgp:2
	v_mfma_scale_f32_16x16x128_f8f6f4 v[130:133], v[8:13], v[206:211], v[130:133], v160, v224 op_sel_hi:[0,0,0] cbsz:2 blgp:2
	v_mfma_scale_f32_16x16x128_f8f6f4 v[126:129], v[2:7], v[206:211], v[126:129], v156, v224 op_sel_hi:[0,0,0] cbsz:2 blgp:2
	v_mfma_scale_f32_16x16x128_f8f6f4 v[114:117], v[8:13], v[212:217], v[114:117], v160, v228 op_sel_hi:[0,0,0] cbsz:2 blgp:2
	v_mfma_scale_f32_16x16x128_f8f6f4 v[110:113], v[2:7], v[212:217], v[110:113], v156, v228 op_sel_hi:[0,0,0] cbsz:2 blgp:2
	v_mfma_scale_f32_16x16x128_f8f6f4 v[98:101], v[8:13], v[218:223], v[98:101], v160, v232 op_sel_hi:[0,0,0] cbsz:2 blgp:2
	v_mfma_scale_f32_16x16x128_f8f6f4 v[94:97], v[2:7], v[218:223], v[94:97], v156, v232 op_sel_hi:[0,0,0] cbsz:2 blgp:2
	s_setprio 0
	s_barrier
	s_add_i32 s64, s42, s27
	s_mov_b32 m0, s64
	ds_read_b128 v[206:209], v204 offset:16384
	ds_read_b128 v[228:231], v204 offset:17408
	ds_read_b128 v[212:215], v204 offset:18432
	ds_read_b128 v[232:235], v204 offset:19456
	ds_read_b128 v[218:221], v204 offset:20480
	ds_read_b128 v[236:239], v204 offset:21504
	ds_read_b128 v[224:227], v204 offset:22528
	ds_read_b128 v[240:243], v204 offset:23552
	global_load_lds_dwordx4 v172, s[22:23]
	s_add_i32 m0, s64, 0x2000
	s_add_u32 s64, s22, 0x40000
	s_addc_u32 s65, s23, 0
	s_add_i32 s66, s43, s27
	global_load_lds_dwordx4 v174, s[22:23]
	s_mov_b32 m0, s66
	s_nop 0
	global_load_lds_dwordx4 v172, s[64:65]
	s_add_i32 m0, s66, 0x2000
	s_nop 0
	global_load_lds_dwordx4 v174, s[64:65]
	s_mov_b32 m0, s35
	s_nop 0
	global_load_lds_dwordx4 v178, s[24:25]
	s_mov_b32 m0, s36
	s_nop 0
	global_load_lds_dwordx4 v176, s[24:25]
	s_add_u32 s98, s22, 0x80
	s_addc_u32 s99, s23, 0
	s_add_u32 s100, s24, 0x80
	s_addc_u32 s101, s25, 0
	s_waitcnt vmcnt(8)
	s_waitcnt lgkmcnt(0)
	s_barrier
	s_setprio 1
	s_waitcnt lgkmcnt(0)
	v_mov_b32_e32 v210, v228
	v_mov_b32_e32 v211, v229
	s_nop 1
	v_mfma_scale_f32_16x16x128_f8f6f4 v[86:89], v[20:25], v[206:211], v[86:89], v168, v230 op_sel_hi:[0,0,0] cbsz:2 blgp:2
	v_mfma_scale_f32_16x16x128_f8f6f4 v[74:77], v[14:19], v[206:211], v[74:77], v164, v230 op_sel_hi:[0,0,0] cbsz:2 blgp:2
	v_mov_b32_e32 v216, v232
	v_mov_b32_e32 v217, v233
	s_nop 1
	v_mfma_scale_f32_16x16x128_f8f6f4 v[70:73], v[20:25], v[212:217], v[70:73], v168, v234 op_sel_hi:[0,0,0] cbsz:2 blgp:2
	v_mfma_scale_f32_16x16x128_f8f6f4 v[58:61], v[14:19], v[212:217], v[58:61], v164, v234 op_sel_hi:[0,0,0] cbsz:2 blgp:2
	v_mov_b32_e32 v222, v236
	v_mov_b32_e32 v223, v237
	s_nop 1
	v_mfma_scale_f32_16x16x128_f8f6f4 v[54:57], v[20:25], v[218:223], v[54:57], v168, v238 op_sel_hi:[0,0,0] cbsz:2 blgp:2
	v_mfma_scale_f32_16x16x128_f8f6f4 v[42:45], v[14:19], v[218:223], v[42:45], v164, v238 op_sel_hi:[0,0,0] cbsz:2 blgp:2
	v_mov_b32_e32 v228, v240
	v_mov_b32_e32 v229, v241
	s_nop 1
	v_mfma_scale_f32_16x16x128_f8f6f4 v[38:41], v[20:25], v[224:229], v[38:41], v168, v242 op_sel_hi:[0,0,0] cbsz:2 blgp:2
	v_mfma_scale_f32_16x16x128_f8f6f4 v[26:29], v[14:19], v[224:229], v[26:29], v164, v242 op_sel_hi:[0,0,0] cbsz:2 blgp:2
	s_setprio 0
	s_setprio 1
	v_mfma_scale_f32_16x16x128_f8f6f4 v[82:85], v[8:13], v[206:211], v[82:85], v160, v230 op_sel_hi:[0,0,0] cbsz:2 blgp:2
	v_mfma_scale_f32_16x16x128_f8f6f4 v[78:81], v[2:7], v[206:211], v[78:81], v156, v230 op_sel_hi:[0,0,0] cbsz:2 blgp:2
	v_mfma_scale_f32_16x16x128_f8f6f4 v[66:69], v[8:13], v[212:217], v[66:69], v160, v234 op_sel_hi:[0,0,0] cbsz:2 blgp:2
	v_mfma_scale_f32_16x16x128_f8f6f4 v[62:65], v[2:7], v[212:217], v[62:65], v156, v234 op_sel_hi:[0,0,0] cbsz:2 blgp:2
	v_mfma_scale_f32_16x16x128_f8f6f4 v[50:53], v[8:13], v[218:223], v[50:53], v160, v238 op_sel_hi:[0,0,0] cbsz:2 blgp:2
	v_mfma_scale_f32_16x16x128_f8f6f4 v[46:49], v[2:7], v[218:223], v[46:49], v156, v238 op_sel_hi:[0,0,0] cbsz:2 blgp:2
	v_mfma_scale_f32_16x16x128_f8f6f4 v[34:37], v[8:13], v[224:229], v[34:37], v160, v242 op_sel_hi:[0,0,0] cbsz:2 blgp:2
	v_mfma_scale_f32_16x16x128_f8f6f4 v[30:33], v[2:7], v[224:229], v[30:33], v156, v242 op_sel_hi:[0,0,0] cbsz:2 blgp:2
	s_setprio 0
	s_barrier
	s_add_i32 s64, 0, 0x18000
	s_add_i32 s65, 0, 0x1c000
	v_add_u32_e32 v2, s64, v198
	v_add_u32_e32 v6, s65, v198
	ds_read_b128 v[20:23], v2
	ds_read_b128 v[166:169], v2 offset:1024
	ds_read_b128 v[14:17], v2 offset:2048
	ds_read_b128 v[162:165], v2 offset:3072
	ds_read_b128 v[8:11], v6
	ds_read_b128 v[154:157], v6 offset:1024
	ds_read_b128 v[2:5], v6 offset:2048
	ds_read_b128 v[158:161], v6 offset:3072
	s_add_u32 s24, s24, 0x40000
	s_addc_u32 s25, s25, 0
	s_mov_b32 m0, s37
	ds_read_b128 v[206:209], v204 offset:32768
	ds_read_b128 v[228:231], v204 offset:33792
	ds_read_b128 v[212:215], v204 offset:34816
	ds_read_b128 v[232:235], v204 offset:35840
	ds_read_b128 v[218:221], v204 offset:36864
	ds_read_b128 v[236:239], v204 offset:37888
	ds_read_b128 v[224:227], v204 offset:38912
	ds_read_b128 v[240:243], v204 offset:39936
	global_load_lds_dwordx4 v178, s[24:25]
	s_mov_b32 m0, s38
	s_nop 0
	global_load_lds_dwordx4 v176, s[24:25]
	s_waitcnt vmcnt(8)
	s_waitcnt lgkmcnt(0)
	s_barrier
	s_setprio 1
	s_waitcnt lgkmcnt(0)
	v_mov_b32_e32 v24, v166
	v_mov_b32_e32 v25, v167
	v_mov_b32_e32 v210, v228
	v_mov_b32_e32 v211, v229
	s_nop 1
	v_mfma_scale_f32_16x16x128_f8f6f4 v[150:153], v[20:25], v[206:211], v[150:153], v168, v230 op_sel_hi:[0,0,0] cbsz:2 blgp:2
	v_mov_b32_e32 v18, v162
	v_mov_b32_e32 v19, v163
	s_nop 1
	v_mfma_scale_f32_16x16x128_f8f6f4 v[138:141], v[14:19], v[206:211], v[138:141], v164, v230 op_sel_hi:[0,0,0] cbsz:2 blgp:2
	v_mov_b32_e32 v216, v232
	v_mov_b32_e32 v217, v233
	s_nop 1
	v_mfma_scale_f32_16x16x128_f8f6f4 v[134:137], v[20:25], v[212:217], v[134:137], v168, v234 op_sel_hi:[0,0,0] cbsz:2 blgp:2
	v_mfma_scale_f32_16x16x128_f8f6f4 v[122:125], v[14:19], v[212:217], v[122:125], v164, v234 op_sel_hi:[0,0,0] cbsz:2 blgp:2
	v_mov_b32_e32 v222, v236
	v_mov_b32_e32 v223, v237
	s_nop 1
	v_mfma_scale_f32_16x16x128_f8f6f4 v[118:121], v[20:25], v[218:223], v[118:121], v168, v238 op_sel_hi:[0,0,0] cbsz:2 blgp:2
	v_mfma_scale_f32_16x16x128_f8f6f4 v[106:109], v[14:19], v[218:223], v[106:109], v164, v238 op_sel_hi:[0,0,0] cbsz:2 blgp:2
	v_mov_b32_e32 v228, v240
	v_mov_b32_e32 v229, v241
	s_nop 1
	v_mfma_scale_f32_16x16x128_f8f6f4 v[102:105], v[20:25], v[224:229], v[102:105], v168, v242 op_sel_hi:[0,0,0] cbsz:2 blgp:2
	v_mfma_scale_f32_16x16x128_f8f6f4 v[90:93], v[14:19], v[224:229], v[90:93], v164, v242 op_sel_hi:[0,0,0] cbsz:2 blgp:2
	s_setprio 0
	s_setprio 1
	v_mov_b32_e32 v12, v154
	v_mov_b32_e32 v13, v155
	s_nop 1
	v_mfma_scale_f32_16x16x128_f8f6f4 v[146:149], v[8:13], v[206:211], v[146:149], v156, v230 op_sel_hi:[0,0,0] cbsz:2 blgp:2
	v_mov_b32_e32 v6, v158
	v_mov_b32_e32 v7, v159
	s_nop 1
	v_mfma_scale_f32_16x16x128_f8f6f4 v[142:145], v[2:7], v[206:211], v[142:145], v160, v230 op_sel_hi:[0,0,0] cbsz:2 blgp:2
	v_mfma_scale_f32_16x16x128_f8f6f4 v[130:133], v[8:13], v[212:217], v[130:133], v156, v234 op_sel_hi:[0,0,0] cbsz:2 blgp:2
	v_mfma_scale_f32_16x16x128_f8f6f4 v[126:129], v[2:7], v[212:217], v[126:129], v160, v234 op_sel_hi:[0,0,0] cbsz:2 blgp:2
	v_mfma_scale_f32_16x16x128_f8f6f4 v[114:117], v[8:13], v[218:223], v[114:117], v156, v238 op_sel_hi:[0,0,0] cbsz:2 blgp:2
	v_mfma_scale_f32_16x16x128_f8f6f4 v[110:113], v[2:7], v[218:223], v[110:113], v160, v238 op_sel_hi:[0,0,0] cbsz:2 blgp:2
	v_mfma_scale_f32_16x16x128_f8f6f4 v[98:101], v[8:13], v[224:229], v[98:101], v156, v242 op_sel_hi:[0,0,0] cbsz:2 blgp:2
	v_mfma_scale_f32_16x16x128_f8f6f4 v[94:97], v[2:7], v[224:229], v[94:97], v160, v242 op_sel_hi:[0,0,0] cbsz:2 blgp:2
	s_setprio 0
	s_barrier
	s_add_i32 s24, s64, s27
	s_mov_b32 m0, s24
	ds_read_b128 v[206:209], v204 offset:49152
	ds_read_b128 v[228:231], v204 offset:50176
	ds_read_b128 v[212:215], v204 offset:51200
	ds_read_b128 v[232:235], v204 offset:52224
	ds_read_b128 v[218:221], v204 offset:53248
	ds_read_b128 v[236:239], v204 offset:54272
	ds_read_b128 v[224:227], v204 offset:55296
	ds_read_b128 v[240:243], v204 offset:56320
	global_load_lds_dwordx4 v172, s[98:99]
	s_add_i32 m0, s24, 0x2000
	s_add_u32 s22, s22, 0x40080
	s_addc_u32 s23, s23, 0
	s_add_i32 s24, s65, s27
	global_load_lds_dwordx4 v174, s[98:99]
	s_mov_b32 m0, s24
	s_nop 0
	global_load_lds_dwordx4 v172, s[22:23]
	s_add_i32 m0, s24, 0x2000
	s_nop 0
	global_load_lds_dwordx4 v174, s[22:23]
	s_mov_b32 m0, s39
	s_nop 0
	global_load_lds_dwordx4 v178, s[100:101]
	s_mov_b32 m0, s40
	s_nop 0
	global_load_lds_dwordx4 v176, s[100:101]
	s_waitcnt vmcnt(8)
	s_waitcnt lgkmcnt(0)
	s_barrier
	s_setprio 1
	s_waitcnt lgkmcnt(0)
	v_mov_b32_e32 v210, v228
	v_mov_b32_e32 v211, v229
	s_nop 1
	v_mfma_scale_f32_16x16x128_f8f6f4 v[86:89], v[20:25], v[206:211], v[86:89], v168, v230 op_sel_hi:[0,0,0] cbsz:2 blgp:2
	v_mfma_scale_f32_16x16x128_f8f6f4 v[74:77], v[14:19], v[206:211], v[74:77], v164, v230 op_sel_hi:[0,0,0] cbsz:2 blgp:2
	v_mov_b32_e32 v216, v232
	v_mov_b32_e32 v217, v233
	s_nop 1
	v_mfma_scale_f32_16x16x128_f8f6f4 v[70:73], v[20:25], v[212:217], v[70:73], v168, v234 op_sel_hi:[0,0,0] cbsz:2 blgp:2
	v_mfma_scale_f32_16x16x128_f8f6f4 v[58:61], v[14:19], v[212:217], v[58:61], v164, v234 op_sel_hi:[0,0,0] cbsz:2 blgp:2
	v_mov_b32_e32 v222, v236
	v_mov_b32_e32 v223, v237
	s_nop 1
	v_mfma_scale_f32_16x16x128_f8f6f4 v[54:57], v[20:25], v[218:223], v[54:57], v168, v238 op_sel_hi:[0,0,0] cbsz:2 blgp:2
	v_mfma_scale_f32_16x16x128_f8f6f4 v[42:45], v[14:19], v[218:223], v[42:45], v164, v238 op_sel_hi:[0,0,0] cbsz:2 blgp:2
	v_mov_b32_e32 v228, v240
	v_mov_b32_e32 v229, v241
	s_nop 1
	v_mfma_scale_f32_16x16x128_f8f6f4 v[38:41], v[20:25], v[224:229], v[38:41], v168, v242 op_sel_hi:[0,0,0] cbsz:2 blgp:2
	v_mfma_scale_f32_16x16x128_f8f6f4 v[26:29], v[14:19], v[224:229], v[26:29], v164, v242 op_sel_hi:[0,0,0] cbsz:2 blgp:2
	s_setprio 0
	s_setprio 1
	v_mfma_scale_f32_16x16x128_f8f6f4 v[82:85], v[8:13], v[206:211], v[82:85], v156, v230 op_sel_hi:[0,0,0] cbsz:2 blgp:2
	v_mfma_scale_f32_16x16x128_f8f6f4 v[78:81], v[2:7], v[206:211], v[78:81], v160, v230 op_sel_hi:[0,0,0] cbsz:2 blgp:2
	v_mfma_scale_f32_16x16x128_f8f6f4 v[66:69], v[8:13], v[212:217], v[66:69], v156, v234 op_sel_hi:[0,0,0] cbsz:2 blgp:2
	v_mfma_scale_f32_16x16x128_f8f6f4 v[62:65], v[2:7], v[212:217], v[62:65], v160, v234 op_sel_hi:[0,0,0] cbsz:2 blgp:2
	v_mfma_scale_f32_16x16x128_f8f6f4 v[50:53], v[8:13], v[218:223], v[50:53], v156, v238 op_sel_hi:[0,0,0] cbsz:2 blgp:2
	v_mfma_scale_f32_16x16x128_f8f6f4 v[46:49], v[2:7], v[218:223], v[46:49], v160, v238 op_sel_hi:[0,0,0] cbsz:2 blgp:2
	v_mfma_scale_f32_16x16x128_f8f6f4 v[34:37], v[8:13], v[224:229], v[34:37], v156, v242 op_sel_hi:[0,0,0] cbsz:2 blgp:2
	v_mfma_scale_f32_16x16x128_f8f6f4 v[30:33], v[2:7], v[224:229], v[30:33], v160, v242 op_sel_hi:[0,0,0] cbsz:2 blgp:2
	s_setprio 0
	s_barrier
	s_add_i32 s63, s63, 2
	s_add_u32 s20, s20, 0x100
	s_addc_u32 s21, s21, 0
	s_add_u32 s61, s61, 0x100
	s_addc_u32 s62, s62, 0
	s_cmp_gt_u32 s63, 13
	s_cbranch_scc0 .LBB0_1257
	s_nop 0
	s_nop 0
	s_nop 0
	s_nop 0
	s_nop 0
	s_nop 0
	s_nop 0
	s_nop 0
	s_and_b64 vcc, exec, s[8:9]
	s_cbranch_vccz .LBB0_1260
	s_barrier

.LBB0_1279:
	ds_read_b128 v[20:23], v195
	ds_read_b128 v[166:169], v195 offset:1024
	ds_read_b128 v[14:17], v195 offset:2048
	ds_read_b128 v[162:165], v195 offset:3072
	ds_read_b128 v[8:11], v196
	ds_read_b128 v[158:161], v196 offset:1024
	ds_read_b128 v[2:5], v196 offset:2048
	ds_read_b128 v[154:157], v196 offset:3072
	s_add_u32 s24, s22, 0xfffc0080
	s_addc_u32 s25, s23, -1
	s_cmp_eq_u32 s61, 12
	s_cselect_b32 s27, s11, s25
	s_cselect_b32 s26, s49, s24
	s_cselect_b32 s25, s13, s60
	s_cselect_b32 s24, s50, s51
	s_mov_b32 m0, s46
	ds_read_b128 v[184:187], v198
	ds_read_b128 v[188:191], v198 offset:1024
	ds_read_b128 v[202:205], v198 offset:2048
	ds_read_b128 v[218:221], v198 offset:3072
	ds_read_b128 v[208:211], v198 offset:4096
	ds_read_b128 v[222:225], v198 offset:5120
	ds_read_b128 v[214:217], v198 offset:6144
	ds_read_b128 v[226:229], v198 offset:7168
	global_load_lds_dwordx4 v180, s[22:23]
	s_add_i32 m0, s21, 0xe000
	s_nop 0
	global_load_lds_dwordx4 v182, s[22:23]
	s_waitcnt vmcnt(8)
	s_waitcnt lgkmcnt(0)
	s_barrier
	s_setprio 1
	s_waitcnt lgkmcnt(0)
	v_mov_b32_e32 v24, v166
	v_mov_b32_e32 v25, v167
	s_nop 1
	v_mfma_scale_f32_16x16x128_f8f6f4 v[150:153], v[20:25], v[184:189], v[150:153], v168, v190 op_sel_hi:[0,0,0] cbsz:2 blgp:2
	v_mov_b32_e32 v18, v162
	v_mov_b32_e32 v19, v163
	s_nop 1
	v_mfma_scale_f32_16x16x128_f8f6f4 v[138:141], v[14:19], v[184:189], v[138:141], v164, v190 op_sel_hi:[0,0,0] cbsz:2 blgp:2
	v_mov_b32_e32 v206, v218
	v_mov_b32_e32 v207, v219
	s_nop 1
	v_mfma_scale_f32_16x16x128_f8f6f4 v[134:137], v[20:25], v[202:207], v[134:137], v168, v220 op_sel_hi:[0,0,0] cbsz:2 blgp:2
	v_mfma_scale_f32_16x16x128_f8f6f4 v[122:125], v[14:19], v[202:207], v[122:125], v164, v220 op_sel_hi:[0,0,0] cbsz:2 blgp:2
	v_mov_b32_e32 v212, v222
	v_mov_b32_e32 v213, v223
	s_nop 1
	v_mfma_scale_f32_16x16x128_f8f6f4 v[118:121], v[20:25], v[208:213], v[118:121], v168, v224 op_sel_hi:[0,0,0] cbsz:2 blgp:2
	v_mfma_scale_f32_16x16x128_f8f6f4 v[106:109], v[14:19], v[208:213], v[106:109], v164, v224 op_sel_hi:[0,0,0] cbsz:2 blgp:2
	v_mov_b32_e32 v218, v226
	v_mov_b32_e32 v219, v227
	s_nop 1
	v_mfma_scale_f32_16x16x128_f8f6f4 v[102:105], v[20:25], v[214:219], v[102:105], v168, v228 op_sel_hi:[0,0,0] cbsz:2 blgp:2
	v_mfma_scale_f32_16x16x128_f8f6f4 v[90:93], v[14:19], v[214:219], v[90:93], v164, v228 op_sel_hi:[0,0,0] cbsz:2 blgp:2
	s_setprio 0
	s_setprio 1
	v_mov_b32_e32 v12, v158
	v_mov_b32_e32 v13, v159
	s_nop 1
	v_mfma_scale_f32_16x16x128_f8f6f4 v[146:149], v[8:13], v[184:189], v[146:149], v160, v190 op_sel_hi:[0,0,0] cbsz:2 blgp:2
	v_mov_b32_e32 v6, v154
	v_mov_b32_e32 v7, v155
	s_nop 1
	v_mfma_scale_f32_16x16x128_f8f6f4 v[142:145], v[2:7], v[184:189], v[142:145], v156, v190 op_sel_hi:[0,0,0] cbsz:2 blgp:2
	v_mfma_scale_f32_16x16x128_f8f6f4 v[130:133], v[8:13], v[202:207], v[130:133], v160, v220 op_sel_hi:[0,0,0] cbsz:2 blgp:2
	v_mfma_scale_f32_16x16x128_f8f6f4 v[126:129], v[2:7], v[202:207], v[126:129], v156, v220 op_sel_hi:[0,0,0] cbsz:2 blgp:2
	v_mfma_scale_f32_16x16x128_f8f6f4 v[114:117], v[8:13], v[208:213], v[114:117], v160, v224 op_sel_hi:[0,0,0] cbsz:2 blgp:2
	v_mfma_scale_f32_16x16x128_f8f6f4 v[110:113], v[2:7], v[208:213], v[110:113], v156, v224 op_sel_hi:[0,0,0] cbsz:2 blgp:2
	v_mfma_scale_f32_16x16x128_f8f6f4 v[98:101], v[8:13], v[214:219], v[98:101], v160, v228 op_sel_hi:[0,0,0] cbsz:2 blgp:2
	v_mfma_scale_f32_16x16x128_f8f6f4 v[94:97], v[2:7], v[214:219], v[94:97], v156, v228 op_sel_hi:[0,0,0] cbsz:2 blgp:2
	s_setprio 0
	s_barrier
	s_add_i32 s62, s42, s35
	s_mov_b32 m0, s62
	ds_read_b128 v[202:205], v198 offset:16384
	ds_read_b128 v[224:227], v198 offset:17408
	ds_read_b128 v[208:211], v198 offset:18432
	ds_read_b128 v[228:231], v198 offset:19456
	ds_read_b128 v[214:217], v198 offset:20480
	ds_read_b128 v[232:235], v198 offset:21504
	ds_read_b128 v[220:223], v198 offset:22528
	ds_read_b128 v[236:239], v198 offset:23552
	global_load_lds_dwordx4 v176, s[24:25]
	s_add_i32 m0, s62, 0x2000
	s_add_u32 s62, s24, 0x40000
	s_addc_u32 s63, s25, 0
	s_add_i32 s64, s43, s35
	global_load_lds_dwordx4 v172, s[24:25]
	s_mov_b32 m0, s64
	s_nop 0
	global_load_lds_dwordx4 v176, s[62:63]
	s_add_i32 m0, s64, 0x2000
	s_nop 0
	global_load_lds_dwordx4 v172, s[62:63]
	s_mov_b32 m0, s21
	s_nop 0
	global_load_lds_dwordx4 v178, s[26:27]
	s_mov_b32 m0, s36
	s_nop 0
	global_load_lds_dwordx4 v174, s[26:27]
	s_add_u32 s98, s24, 0x80
	s_addc_u32 s99, s25, 0
	s_add_u32 s100, s26, 0x80
	s_addc_u32 s101, s27, 0
	s_waitcnt vmcnt(8)
	s_waitcnt lgkmcnt(0)
	s_barrier
	s_setprio 1
	s_waitcnt lgkmcnt(0)
	v_mov_b32_e32 v206, v224
	v_mov_b32_e32 v207, v225
	s_nop 1
	v_mfma_scale_f32_16x16x128_f8f6f4 v[86:89], v[20:25], v[202:207], v[86:89], v168, v226 op_sel_hi:[0,0,0] cbsz:2 blgp:2
	v_mfma_scale_f32_16x16x128_f8f6f4 v[74:77], v[14:19], v[202:207], v[74:77], v164, v226 op_sel_hi:[0,0,0] cbsz:2 blgp:2
	v_mov_b32_e32 v212, v228
	v_mov_b32_e32 v213, v229
	s_nop 1
	v_mfma_scale_f32_16x16x128_f8f6f4 v[70:73], v[20:25], v[208:213], v[70:73], v168, v230 op_sel_hi:[0,0,0] cbsz:2 blgp:2
	v_mfma_scale_f32_16x16x128_f8f6f4 v[58:61], v[14:19], v[208:213], v[58:61], v164, v230 op_sel_hi:[0,0,0] cbsz:2 blgp:2
	v_mov_b32_e32 v218, v232
	v_mov_b32_e32 v219, v233
	s_nop 1
	v_mfma_scale_f32_16x16x128_f8f6f4 v[54:57], v[20:25], v[214:219], v[54:57], v168, v234 op_sel_hi:[0,0,0] cbsz:2 blgp:2
	v_mfma_scale_f32_16x16x128_f8f6f4 v[42:45], v[14:19], v[214:219], v[42:45], v164, v234 op_sel_hi:[0,0,0] cbsz:2 blgp:2
	v_mov_b32_e32 v224, v236
	v_mov_b32_e32 v225, v237
	s_nop 1
	v_mfma_scale_f32_16x16x128_f8f6f4 v[38:41], v[20:25], v[220:225], v[38:41], v168, v238 op_sel_hi:[0,0,0] cbsz:2 blgp:2
	v_mfma_scale_f32_16x16x128_f8f6f4 v[26:29], v[14:19], v[220:225], v[26:29], v164, v238 op_sel_hi:[0,0,0] cbsz:2 blgp:2
	s_setprio 0
	s_setprio 1
	v_mfma_scale_f32_16x16x128_f8f6f4 v[82:85], v[8:13], v[202:207], v[82:85], v160, v226 op_sel_hi:[0,0,0] cbsz:2 blgp:2
	v_mfma_scale_f32_16x16x128_f8f6f4 v[78:81], v[2:7], v[202:207], v[78:81], v156, v226 op_sel_hi:[0,0,0] cbsz:2 blgp:2
	v_mfma_scale_f32_16x16x128_f8f6f4 v[66:69], v[8:13], v[208:213], v[66:69], v160, v230 op_sel_hi:[0,0,0] cbsz:2 blgp:2
	v_mfma_scale_f32_16x16x128_f8f6f4 v[62:65], v[2:7], v[208:213], v[62:65], v156, v230 op_sel_hi:[0,0,0] cbsz:2 blgp:2
	v_mfma_scale_f32_16x16x128_f8f6f4 v[50:53], v[8:13], v[214:219], v[50:53], v160, v234 op_sel_hi:[0,0,0] cbsz:2 blgp:2
	v_mfma_scale_f32_16x16x128_f8f6f4 v[46:49], v[2:7], v[214:219], v[46:49], v156, v234 op_sel_hi:[0,0,0] cbsz:2 blgp:2
	v_mfma_scale_f32_16x16x128_f8f6f4 v[34:37], v[8:13], v[220:225], v[34:37], v160, v238 op_sel_hi:[0,0,0] cbsz:2 blgp:2
	v_mfma_scale_f32_16x16x128_f8f6f4 v[30:33], v[2:7], v[220:225], v[30:33], v156, v238 op_sel_hi:[0,0,0] cbsz:2 blgp:2
	s_setprio 0
	s_barrier
	s_add_i32 s62, 0, 0x18000
	s_add_i32 s63, 0, 0x1c000
	v_add_u32_e32 v2, s62, v194
	v_add_u32_e32 v6, s63, v194
	ds_read_b128 v[20:23], v2
	ds_read_b128 v[166:169], v2 offset:1024
	ds_read_b128 v[14:17], v2 offset:2048
	ds_read_b128 v[162:165], v2 offset:3072
	ds_read_b128 v[8:11], v6
	ds_read_b128 v[154:157], v6 offset:1024
	ds_read_b128 v[2:5], v6 offset:2048
	ds_read_b128 v[158:161], v6 offset:3072
	s_add_u32 s26, s26, 0x40000
	s_addc_u32 s27, s27, 0
	s_mov_b32 m0, s37
	ds_read_b128 v[202:205], v198 offset:32768
	ds_read_b128 v[224:227], v198 offset:33792
	ds_read_b128 v[208:211], v198 offset:34816
	ds_read_b128 v[228:231], v198 offset:35840
	ds_read_b128 v[214:217], v198 offset:36864
	ds_read_b128 v[232:235], v198 offset:37888
	ds_read_b128 v[220:223], v198 offset:38912
	ds_read_b128 v[236:239], v198 offset:39936
	global_load_lds_dwordx4 v178, s[26:27]
	s_mov_b32 m0, s38
	s_nop 0
	global_load_lds_dwordx4 v174, s[26:27]
	s_waitcnt vmcnt(8)
	s_waitcnt lgkmcnt(0)
	s_barrier
	s_setprio 1
	s_waitcnt lgkmcnt(0)
	v_mov_b32_e32 v24, v166
	v_mov_b32_e32 v25, v167
	v_mov_b32_e32 v206, v224
	v_mov_b32_e32 v207, v225
	s_nop 1
	v_mfma_scale_f32_16x16x128_f8f6f4 v[150:153], v[20:25], v[202:207], v[150:153], v168, v226 op_sel_hi:[0,0,0] cbsz:2 blgp:2
	v_mov_b32_e32 v18, v162
	v_mov_b32_e32 v19, v163
	s_nop 1
	v_mfma_scale_f32_16x16x128_f8f6f4 v[138:141], v[14:19], v[202:207], v[138:141], v164, v226 op_sel_hi:[0,0,0] cbsz:2 blgp:2
	v_mov_b32_e32 v212, v228
	v_mov_b32_e32 v213, v229
	s_nop 1
	v_mfma_scale_f32_16x16x128_f8f6f4 v[134:137], v[20:25], v[208:213], v[134:137], v168, v230 op_sel_hi:[0,0,0] cbsz:2 blgp:2
	v_mfma_scale_f32_16x16x128_f8f6f4 v[122:125], v[14:19], v[208:213], v[122:125], v164, v230 op_sel_hi:[0,0,0] cbsz:2 blgp:2
	v_mov_b32_e32 v218, v232
	v_mov_b32_e32 v219, v233
	s_nop 1
	v_mfma_scale_f32_16x16x128_f8f6f4 v[118:121], v[20:25], v[214:219], v[118:121], v168, v234 op_sel_hi:[0,0,0] cbsz:2 blgp:2
	v_mfma_scale_f32_16x16x128_f8f6f4 v[106:109], v[14:19], v[214:219], v[106:109], v164, v234 op_sel_hi:[0,0,0] cbsz:2 blgp:2
	v_mov_b32_e32 v224, v236
	v_mov_b32_e32 v225, v237
	s_nop 1
	v_mfma_scale_f32_16x16x128_f8f6f4 v[102:105], v[20:25], v[220:225], v[102:105], v168, v238 op_sel_hi:[0,0,0] cbsz:2 blgp:2
	v_mfma_scale_f32_16x16x128_f8f6f4 v[90:93], v[14:19], v[220:225], v[90:93], v164, v238 op_sel_hi:[0,0,0] cbsz:2 blgp:2
	s_setprio 0
	s_setprio 1
	v_mov_b32_e32 v12, v154
	v_mov_b32_e32 v13, v155
	s_nop 1
	v_mfma_scale_f32_16x16x128_f8f6f4 v[146:149], v[8:13], v[202:207], v[146:149], v156, v226 op_sel_hi:[0,0,0] cbsz:2 blgp:2
	v_mov_b32_e32 v6, v158
	v_mov_b32_e32 v7, v159
	s_nop 1
	v_mfma_scale_f32_16x16x128_f8f6f4 v[142:145], v[2:7], v[202:207], v[142:145], v160, v226 op_sel_hi:[0,0,0] cbsz:2 blgp:2
	v_mfma_scale_f32_16x16x128_f8f6f4 v[130:133], v[8:13], v[208:213], v[130:133], v156, v230 op_sel_hi:[0,0,0] cbsz:2 blgp:2
	v_mfma_scale_f32_16x16x128_f8f6f4 v[126:129], v[2:7], v[208:213], v[126:129], v160, v230 op_sel_hi:[0,0,0] cbsz:2 blgp:2
	v_mfma_scale_f32_16x16x128_f8f6f4 v[114:117], v[8:13], v[214:219], v[114:117], v156, v234 op_sel_hi:[0,0,0] cbsz:2 blgp:2
	v_mfma_scale_f32_16x16x128_f8f6f4 v[110:113], v[2:7], v[214:219], v[110:113], v160, v234 op_sel_hi:[0,0,0] cbsz:2 blgp:2
	v_mfma_scale_f32_16x16x128_f8f6f4 v[98:101], v[8:13], v[220:225], v[98:101], v156, v238 op_sel_hi:[0,0,0] cbsz:2 blgp:2
	v_mfma_scale_f32_16x16x128_f8f6f4 v[94:97], v[2:7], v[220:225], v[94:97], v160, v238 op_sel_hi:[0,0,0] cbsz:2 blgp:2
	s_setprio 0
	s_barrier
	s_add_i32 s26, s62, s35
	s_mov_b32 m0, s26
	ds_read_b128 v[202:205], v198 offset:49152
	ds_read_b128 v[224:227], v198 offset:50176
	ds_read_b128 v[208:211], v198 offset:51200
	ds_read_b128 v[228:231], v198 offset:52224
	ds_read_b128 v[214:217], v198 offset:53248
	ds_read_b128 v[232:235], v198 offset:54272
	ds_read_b128 v[220:223], v198 offset:55296
	ds_read_b128 v[236:239], v198 offset:56320
	global_load_lds_dwordx4 v176, s[98:99]
	s_add_i32 m0, s26, 0x2000
	s_add_u32 s24, s24, 0x40080
	s_addc_u32 s25, s25, 0
	s_add_i32 s26, s63, s35
	global_load_lds_dwordx4 v172, s[98:99]
	s_mov_b32 m0, s26
	s_nop 0
	global_load_lds_dwordx4 v176, s[24:25]
	s_add_i32 m0, s26, 0x2000
	s_nop 0
	global_load_lds_dwordx4 v172, s[24:25]
	s_mov_b32 m0, s40
	s_nop 0
	global_load_lds_dwordx4 v178, s[100:101]
	s_mov_b32 m0, s41
	s_nop 0
	global_load_lds_dwordx4 v174, s[100:101]
	s_waitcnt vmcnt(8)
	s_waitcnt lgkmcnt(0)
	s_barrier
	s_setprio 1
	s_waitcnt lgkmcnt(0)
	v_mov_b32_e32 v206, v224
	v_mov_b32_e32 v207, v225
	s_nop 1
	v_mfma_scale_f32_16x16x128_f8f6f4 v[86:89], v[20:25], v[202:207], v[86:89], v168, v226 op_sel_hi:[0,0,0] cbsz:2 blgp:2
	v_mfma_scale_f32_16x16x128_f8f6f4 v[74:77], v[14:19], v[202:207], v[74:77], v164, v226 op_sel_hi:[0,0,0] cbsz:2 blgp:2
	v_mov_b32_e32 v212, v228
	v_mov_b32_e32 v213, v229
	s_nop 1
	v_mfma_scale_f32_16x16x128_f8f6f4 v[70:73], v[20:25], v[208:213], v[70:73], v168, v230 op_sel_hi:[0,0,0] cbsz:2 blgp:2
	v_mfma_scale_f32_16x16x128_f8f6f4 v[58:61], v[14:19], v[208:213], v[58:61], v164, v230 op_sel_hi:[0,0,0] cbsz:2 blgp:2
	v_mov_b32_e32 v218, v232
	v_mov_b32_e32 v219, v233
	s_nop 1
	v_mfma_scale_f32_16x16x128_f8f6f4 v[54:57], v[20:25], v[214:219], v[54:57], v168, v234 op_sel_hi:[0,0,0] cbsz:2 blgp:2
	v_mfma_scale_f32_16x16x128_f8f6f4 v[42:45], v[14:19], v[214:219], v[42:45], v164, v234 op_sel_hi:[0,0,0] cbsz:2 blgp:2
	v_mov_b32_e32 v224, v236
	v_mov_b32_e32 v225, v237
	s_nop 1
	v_mfma_scale_f32_16x16x128_f8f6f4 v[38:41], v[20:25], v[220:225], v[38:41], v168, v238 op_sel_hi:[0,0,0] cbsz:2 blgp:2
	v_mfma_scale_f32_16x16x128_f8f6f4 v[26:29], v[14:19], v[220:225], v[26:29], v164, v238 op_sel_hi:[0,0,0] cbsz:2 blgp:2
	s_setprio 0
	s_setprio 1
	v_mfma_scale_f32_16x16x128_f8f6f4 v[82:85], v[8:13], v[202:207], v[82:85], v156, v226 op_sel_hi:[0,0,0] cbsz:2 blgp:2
	v_mfma_scale_f32_16x16x128_f8f6f4 v[78:81], v[2:7], v[202:207], v[78:81], v160, v226 op_sel_hi:[0,0,0] cbsz:2 blgp:2
	v_mfma_scale_f32_16x16x128_f8f6f4 v[66:69], v[8:13], v[208:213], v[66:69], v156, v230 op_sel_hi:[0,0,0] cbsz:2 blgp:2
	v_mfma_scale_f32_16x16x128_f8f6f4 v[62:65], v[2:7], v[208:213], v[62:65], v160, v230 op_sel_hi:[0,0,0] cbsz:2 blgp:2
	v_mfma_scale_f32_16x16x128_f8f6f4 v[50:53], v[8:13], v[214:219], v[50:53], v156, v234 op_sel_hi:[0,0,0] cbsz:2 blgp:2
	v_mfma_scale_f32_16x16x128_f8f6f4 v[46:49], v[2:7], v[214:219], v[46:49], v160, v234 op_sel_hi:[0,0,0] cbsz:2 blgp:2
	v_mfma_scale_f32_16x16x128_f8f6f4 v[34:37], v[8:13], v[220:225], v[34:37], v156, v238 op_sel_hi:[0,0,0] cbsz:2 blgp:2
	v_mfma_scale_f32_16x16x128_f8f6f4 v[30:33], v[2:7], v[220:225], v[30:33], v160, v238 op_sel_hi:[0,0,0] cbsz:2 blgp:2
	s_setprio 0
	s_barrier
	s_add_i32 s61, s61, 2
	s_add_u32 s22, s22, 0x100
	s_addc_u32 s23, s23, 0
	s_add_u32 s51, s51, 0x100
	s_addc_u32 s60, s60, 0
	s_cmp_gt_u32 s61, 13
	s_cbranch_scc0 .LBB0_1279
	s_nop 0
	s_nop 0
	s_nop 0
	s_nop 0
	s_nop 0
	s_nop 0
	s_nop 0
	s_nop 0
	s_and_b64 vcc, exec, s[8:9]
	s_cbranch_vccz .LBB0_1282
	s_barrier

.LBB0_1391:
	ds_read_b128 v[24:27], v186
	ds_read_b128 v[28:31], v186 offset:1024
	ds_read_b128 v[16:19], v186 offset:2048
	ds_read_b128 v[20:23], v186 offset:3072
	ds_read_b128 v[8:11], v187
	ds_read_b128 v[12:15], v187 offset:1024
	ds_read_b128 v[0:3], v187 offset:2048
	ds_read_b128 v[4:7], v187 offset:3072
	s_add_u32 s26, s24, 0xfff20080
	s_addc_u32 s27, s25, -1
	s_cmp_eq_u32 s67, 52
	s_cselect_b32 s29, s23, s27
	s_cselect_b32 s28, s22, s26
	s_cselect_b32 s27, s1, s66
	s_cselect_b32 s26, s0, s65
	s_add_i32 m0, s36, 0xc000
	ds_read_b128 v[174:177], v188
	ds_read_b128 v[178:181], v188 offset:1024
	ds_read_b128 v[192:195], v188 offset:2048
	ds_read_b128 v[196:199], v188 offset:3072
	ds_read_b128 v[202:205], v188 offset:4096
	ds_read_b128 v[206:209], v188 offset:5120
	ds_read_b128 v[210:213], v188 offset:6144
	ds_read_b128 v[214:217], v188 offset:7168
	global_load_lds_dwordx4 v170, s[24:25]
	s_add_i32 m0, s36, 0xe000
	s_nop 0
	global_load_lds_dwordx4 v172, s[24:25]
	s_waitcnt vmcnt(8)
	s_waitcnt lgkmcnt(0)
	s_barrier
	s_setprio 1
	s_waitcnt lgkmcnt(0)
	v_mfma_scale_f32_16x16x128_f8f6f4 v[156:159], v[24:31], v[174:181], v[156:159], v189, v190 op_sel_hi:[0,0,0]
	v_mfma_scale_f32_16x16x128_f8f6f4 v[152:155], v[16:23], v[174:181], v[152:155], v189, v190 op_sel_hi:[0,0,0]
	v_mfma_scale_f32_16x16x128_f8f6f4 v[140:143], v[24:31], v[192:199], v[140:143], v189, v190 op_sel_hi:[0,0,0]
	v_mfma_scale_f32_16x16x128_f8f6f4 v[136:139], v[16:23], v[192:199], v[136:139], v189, v190 op_sel_hi:[0,0,0]
	v_mfma_scale_f32_16x16x128_f8f6f4 v[124:127], v[24:31], v[202:209], v[124:127], v189, v190 op_sel_hi:[0,0,0]
	v_mfma_scale_f32_16x16x128_f8f6f4 v[120:123], v[16:23], v[202:209], v[120:123], v189, v190 op_sel_hi:[0,0,0]
	v_mfma_scale_f32_16x16x128_f8f6f4 v[108:111], v[24:31], v[210:217], v[108:111], v189, v190 op_sel_hi:[0,0,0]
	v_mfma_scale_f32_16x16x128_f8f6f4 v[104:107], v[16:23], v[210:217], v[104:107], v189, v190 op_sel_hi:[0,0,0]
	s_setprio 0
	s_setprio 1
	v_mfma_scale_f32_16x16x128_f8f6f4 v[148:151], v[8:15], v[174:181], v[148:151], v189, v190 op_sel_hi:[0,0,0]
	v_mfma_scale_f32_16x16x128_f8f6f4 v[144:147], v[0:7], v[174:181], v[144:147], v189, v190 op_sel_hi:[0,0,0]
	v_mfma_scale_f32_16x16x128_f8f6f4 v[132:135], v[8:15], v[192:199], v[132:135], v189, v190 op_sel_hi:[0,0,0]
	v_mfma_scale_f32_16x16x128_f8f6f4 v[128:131], v[0:7], v[192:199], v[128:131], v189, v190 op_sel_hi:[0,0,0]
	v_mfma_scale_f32_16x16x128_f8f6f4 v[116:119], v[8:15], v[202:209], v[116:119], v189, v190 op_sel_hi:[0,0,0]
	v_mfma_scale_f32_16x16x128_f8f6f4 v[112:115], v[0:7], v[202:209], v[112:115], v189, v190 op_sel_hi:[0,0,0]
	v_mfma_scale_f32_16x16x128_f8f6f4 v[100:103], v[8:15], v[210:217], v[100:103], v189, v190 op_sel_hi:[0,0,0]
	v_mfma_scale_f32_16x16x128_f8f6f4 v[96:99], v[0:7], v[210:217], v[96:99], v189, v190 op_sel_hi:[0,0,0]
	s_setprio 0
	s_barrier
	s_add_i32 s68, s44, s35
	s_mov_b32 m0, s68
	ds_read_b128 v[192:195], v188 offset:16384
	ds_read_b128 v[196:199], v188 offset:17408
	ds_read_b128 v[202:205], v188 offset:18432
	ds_read_b128 v[206:209], v188 offset:19456
	ds_read_b128 v[210:213], v188 offset:20480
	ds_read_b128 v[214:217], v188 offset:21504
	ds_read_b128 v[218:221], v188 offset:22528
	ds_read_b128 v[222:225], v188 offset:23552
	global_load_lds_dwordx4 v160, s[26:27]
	s_add_i32 m0, s68, 0x2000
	s_add_u32 s68, s26, 0xe0000
	s_addc_u32 s69, s27, 0
	s_add_i32 s70, s45, s35
	global_load_lds_dwordx4 v164, s[26:27]
	s_mov_b32 m0, s70
	s_nop 0
	global_load_lds_dwordx4 v160, s[68:69]
	s_add_i32 m0, s70, 0x2000
	s_nop 0
	global_load_lds_dwordx4 v164, s[68:69]
	s_mov_b32 m0, s36
	s_nop 0
	global_load_lds_dwordx4 v168, s[28:29]
	s_mov_b32 m0, s37
	s_nop 0
	global_load_lds_dwordx4 v166, s[28:29]
	s_add_u32 s98, s26, 0x80
	s_addc_u32 s99, s27, 0
	s_add_u32 s100, s28, 0x80
	s_addc_u32 s101, s29, 0
	s_waitcnt vmcnt(8)
	s_waitcnt lgkmcnt(0)
	s_barrier
	s_setprio 1
	s_waitcnt lgkmcnt(0)
	v_mfma_scale_f32_16x16x128_f8f6f4 v[92:95], v[24:31], v[192:199], v[92:95], v189, v190 op_sel_hi:[0,0,0]
	v_mfma_scale_f32_16x16x128_f8f6f4 v[88:91], v[16:23], v[192:199], v[88:91], v189, v190 op_sel_hi:[0,0,0]
	v_mfma_scale_f32_16x16x128_f8f6f4 v[76:79], v[24:31], v[202:209], v[76:79], v189, v190 op_sel_hi:[0,0,0]
	v_mfma_scale_f32_16x16x128_f8f6f4 v[72:75], v[16:23], v[202:209], v[72:75], v189, v190 op_sel_hi:[0,0,0]
	v_mfma_scale_f32_16x16x128_f8f6f4 v[60:63], v[24:31], v[210:217], v[60:63], v189, v190 op_sel_hi:[0,0,0]
	v_mfma_scale_f32_16x16x128_f8f6f4 v[56:59], v[16:23], v[210:217], v[56:59], v189, v190 op_sel_hi:[0,0,0]
	v_mfma_scale_f32_16x16x128_f8f6f4 v[44:47], v[24:31], v[218:225], v[44:47], v189, v190 op_sel_hi:[0,0,0]
	v_mfma_scale_f32_16x16x128_f8f6f4 v[40:43], v[16:23], v[218:225], v[40:43], v189, v190 op_sel_hi:[0,0,0]
	s_setprio 0
	s_setprio 1
	v_mfma_scale_f32_16x16x128_f8f6f4 v[84:87], v[8:15], v[192:199], v[84:87], v189, v190 op_sel_hi:[0,0,0]
	v_mfma_scale_f32_16x16x128_f8f6f4 v[80:83], v[0:7], v[192:199], v[80:83], v189, v190 op_sel_hi:[0,0,0]
	v_mfma_scale_f32_16x16x128_f8f6f4 v[68:71], v[8:15], v[202:209], v[68:71], v189, v190 op_sel_hi:[0,0,0]
	v_mfma_scale_f32_16x16x128_f8f6f4 v[64:67], v[0:7], v[202:209], v[64:67], v189, v190 op_sel_hi:[0,0,0]
	v_mfma_scale_f32_16x16x128_f8f6f4 v[52:55], v[8:15], v[210:217], v[52:55], v189, v190 op_sel_hi:[0,0,0]
	v_mfma_scale_f32_16x16x128_f8f6f4 v[48:51], v[0:7], v[210:217], v[48:51], v189, v190 op_sel_hi:[0,0,0]
	v_mfma_scale_f32_16x16x128_f8f6f4 v[36:39], v[8:15], v[218:225], v[36:39], v189, v190 op_sel_hi:[0,0,0]
	v_mfma_scale_f32_16x16x128_f8f6f4 v[32:35], v[0:7], v[218:225], v[32:35], v189, v190 op_sel_hi:[0,0,0]
	s_setprio 0
	s_barrier
	s_add_i32 s68, 0, 0x18000
	s_add_i32 s69, 0, 0x1c000
	v_add_u32_e32 v12, s68, v184
	v_add_u32_e32 v28, s69, v184
	ds_read_b128 v[0:3], v12
	ds_read_b128 v[4:7], v12 offset:1024
	ds_read_b128 v[8:11], v12 offset:2048
	ds_read_b128 v[12:15], v12 offset:3072
	ds_read_b128 v[16:19], v28
	ds_read_b128 v[20:23], v28 offset:1024
	ds_read_b128 v[24:27], v28 offset:2048
	ds_read_b128 v[28:31], v28 offset:3072
	s_add_u32 s28, s28, 0xe0000
	s_addc_u32 s29, s29, 0
	s_mov_b32 m0, s38
	ds_read_b128 v[192:195], v188 offset:32768
	ds_read_b128 v[196:199], v188 offset:33792
	ds_read_b128 v[202:205], v188 offset:34816
	ds_read_b128 v[206:209], v188 offset:35840
	ds_read_b128 v[210:213], v188 offset:36864
	ds_read_b128 v[214:217], v188 offset:37888
	ds_read_b128 v[218:221], v188 offset:38912
	ds_read_b128 v[222:225], v188 offset:39936
	global_load_lds_dwordx4 v168, s[28:29]
	s_mov_b32 m0, s39
	s_nop 0
	global_load_lds_dwordx4 v166, s[28:29]
	s_waitcnt vmcnt(8)
	s_waitcnt lgkmcnt(0)
	s_barrier
	s_setprio 1
	s_waitcnt lgkmcnt(0)
	v_mfma_scale_f32_16x16x128_f8f6f4 v[156:159], v[0:7], v[192:199], v[156:159], v189, v190 op_sel_hi:[0,0,0]
	v_mfma_scale_f32_16x16x128_f8f6f4 v[152:155], v[8:15], v[192:199], v[152:155], v189, v190 op_sel_hi:[0,0,0]
	v_mfma_scale_f32_16x16x128_f8f6f4 v[140:143], v[0:7], v[202:209], v[140:143], v189, v190 op_sel_hi:[0,0,0]
	v_mfma_scale_f32_16x16x128_f8f6f4 v[136:139], v[8:15], v[202:209], v[136:139], v189, v190 op_sel_hi:[0,0,0]
	v_mfma_scale_f32_16x16x128_f8f6f4 v[124:127], v[0:7], v[210:217], v[124:127], v189, v190 op_sel_hi:[0,0,0]
	v_mfma_scale_f32_16x16x128_f8f6f4 v[120:123], v[8:15], v[210:217], v[120:123], v189, v190 op_sel_hi:[0,0,0]
	v_mfma_scale_f32_16x16x128_f8f6f4 v[108:111], v[0:7], v[218:225], v[108:111], v189, v190 op_sel_hi:[0,0,0]
	v_mfma_scale_f32_16x16x128_f8f6f4 v[104:107], v[8:15], v[218:225], v[104:107], v189, v190 op_sel_hi:[0,0,0]
	s_setprio 0
	s_setprio 1
	v_mfma_scale_f32_16x16x128_f8f6f4 v[148:151], v[16:23], v[192:199], v[148:151], v189, v190 op_sel_hi:[0,0,0]
	v_mfma_scale_f32_16x16x128_f8f6f4 v[144:147], v[24:31], v[192:199], v[144:147], v189, v190 op_sel_hi:[0,0,0]
	v_mfma_scale_f32_16x16x128_f8f6f4 v[132:135], v[16:23], v[202:209], v[132:135], v189, v190 op_sel_hi:[0,0,0]
	v_mfma_scale_f32_16x16x128_f8f6f4 v[128:131], v[24:31], v[202:209], v[128:131], v189, v190 op_sel_hi:[0,0,0]
	v_mfma_scale_f32_16x16x128_f8f6f4 v[116:119], v[16:23], v[210:217], v[116:119], v189, v190 op_sel_hi:[0,0,0]
	v_mfma_scale_f32_16x16x128_f8f6f4 v[112:115], v[24:31], v[210:217], v[112:115], v189, v190 op_sel_hi:[0,0,0]
	v_mfma_scale_f32_16x16x128_f8f6f4 v[100:103], v[16:23], v[218:225], v[100:103], v189, v190 op_sel_hi:[0,0,0]
	v_mfma_scale_f32_16x16x128_f8f6f4 v[96:99], v[24:31], v[218:225], v[96:99], v189, v190 op_sel_hi:[0,0,0]
	s_setprio 0
	s_barrier
	s_add_i32 s28, s68, s35
	s_mov_b32 m0, s28
	ds_read_b128 v[192:195], v188 offset:49152
	ds_read_b128 v[196:199], v188 offset:50176
	ds_read_b128 v[202:205], v188 offset:51200
	ds_read_b128 v[206:209], v188 offset:52224
	ds_read_b128 v[210:213], v188 offset:53248
	ds_read_b128 v[214:217], v188 offset:54272
	ds_read_b128 v[218:221], v188 offset:55296
	ds_read_b128 v[222:225], v188 offset:56320
	global_load_lds_dwordx4 v160, s[98:99]
	s_add_i32 m0, s28, 0x2000
	s_add_u32 s26, s26, 0xe0080
	s_addc_u32 s27, s27, 0
	s_add_i32 s28, s69, s35
	global_load_lds_dwordx4 v164, s[98:99]
	s_mov_b32 m0, s28
	s_nop 0
	global_load_lds_dwordx4 v160, s[26:27]
	s_add_i32 m0, s28, 0x2000
	s_nop 0
	global_load_lds_dwordx4 v164, s[26:27]
	s_mov_b32 m0, s41
	s_nop 0
	global_load_lds_dwordx4 v168, s[100:101]
	s_mov_b32 m0, s42
	s_nop 0
	global_load_lds_dwordx4 v166, s[100:101]
	s_waitcnt vmcnt(8)
	s_waitcnt lgkmcnt(0)
	s_barrier
	s_setprio 1
	s_waitcnt lgkmcnt(0)
	v_mfma_scale_f32_16x16x128_f8f6f4 v[92:95], v[0:7], v[192:199], v[92:95], v189, v190 op_sel_hi:[0,0,0]
	v_mfma_scale_f32_16x16x128_f8f6f4 v[88:91], v[8:15], v[192:199], v[88:91], v189, v190 op_sel_hi:[0,0,0]
	v_mfma_scale_f32_16x16x128_f8f6f4 v[76:79], v[0:7], v[202:209], v[76:79], v189, v190 op_sel_hi:[0,0,0]
	v_mfma_scale_f32_16x16x128_f8f6f4 v[72:75], v[8:15], v[202:209], v[72:75], v189, v190 op_sel_hi:[0,0,0]
	v_mfma_scale_f32_16x16x128_f8f6f4 v[60:63], v[0:7], v[210:217], v[60:63], v189, v190 op_sel_hi:[0,0,0]
	v_mfma_scale_f32_16x16x128_f8f6f4 v[56:59], v[8:15], v[210:217], v[56:59], v189, v190 op_sel_hi:[0,0,0]
	v_mfma_scale_f32_16x16x128_f8f6f4 v[44:47], v[0:7], v[218:225], v[44:47], v189, v190 op_sel_hi:[0,0,0]
	v_mfma_scale_f32_16x16x128_f8f6f4 v[40:43], v[8:15], v[218:225], v[40:43], v189, v190 op_sel_hi:[0,0,0]
	s_setprio 0
	s_setprio 1
	v_mfma_scale_f32_16x16x128_f8f6f4 v[84:87], v[16:23], v[192:199], v[84:87], v189, v190 op_sel_hi:[0,0,0]
	v_mfma_scale_f32_16x16x128_f8f6f4 v[80:83], v[24:31], v[192:199], v[80:83], v189, v190 op_sel_hi:[0,0,0]
	v_mfma_scale_f32_16x16x128_f8f6f4 v[68:71], v[16:23], v[202:209], v[68:71], v189, v190 op_sel_hi:[0,0,0]
	v_mfma_scale_f32_16x16x128_f8f6f4 v[64:67], v[24:31], v[202:209], v[64:67], v189, v190 op_sel_hi:[0,0,0]
	v_mfma_scale_f32_16x16x128_f8f6f4 v[52:55], v[16:23], v[210:217], v[52:55], v189, v190 op_sel_hi:[0,0,0]
	v_mfma_scale_f32_16x16x128_f8f6f4 v[48:51], v[24:31], v[210:217], v[48:51], v189, v190 op_sel_hi:[0,0,0]
	v_mfma_scale_f32_16x16x128_f8f6f4 v[36:39], v[16:23], v[218:225], v[36:39], v189, v190 op_sel_hi:[0,0,0]
	v_mfma_scale_f32_16x16x128_f8f6f4 v[32:35], v[24:31], v[218:225], v[32:35], v189, v190 op_sel_hi:[0,0,0]
	s_setprio 0
	s_barrier
	s_add_i32 s67, s67, 2
	s_add_u32 s24, s24, 0x100
	s_addc_u32 s25, s25, 0
	s_add_u32 s65, s65, 0x100
	s_addc_u32 s66, s66, 0
	s_cmp_gt_u32 s67, 53
	s_cbranch_scc0 .LBB0_1391
	s_nop 0
	s_nop 0
	s_nop 0
	s_nop 0
	s_nop 0
	s_nop 0
	s_nop 0
	s_nop 0
	s_nop 0
	s_and_b64 vcc, exec, s[10:11]
	s_cbranch_vccz .LBB0_1394
	s_barrier
